# row loops NORM_A, NORM_B, NORM_C: next-row loads kept in flight during compute (unpack moved to loop bottom, counted waits, gain-vector waits hoisted before the loops)
# speedup vs baseline: 1.0039x; 1.0001x over previous
.LBB0_1626:
	s_or_b64 exec, exec, s[14:15]
	s_and_b64 vcc, exec, s[12:13]
	s_cbranch_vccnz .Lnb_no_next
	s_waitcnt vmcnt(23)
	v_lshlrev_b32_e32 v105, 16, v110
	v_and_b32_e32 v106, 0xffff0000, v110
	v_lshlrev_b32_e32 v107, 16, v111
	v_and_b32_e32 v108, 0xffff0000, v111
	s_waitcnt vmcnt(22)
	v_lshlrev_b32_e32 v109, 16, v112
	v_and_b32_e32 v110, 0xffff0000, v112
	v_lshlrev_b32_e32 v111, 16, v113
	v_and_b32_e32 v112, 0xffff0000, v113
	s_waitcnt vmcnt(21)
	v_lshlrev_b32_e32 v113, 16, v116
	v_and_b32_e32 v114, 0xffff0000, v116
	v_lshlrev_b32_e32 v115, 16, v117
	v_and_b32_e32 v116, 0xffff0000, v117
	s_waitcnt vmcnt(20)
	v_lshlrev_b32_e32 v117, 16, v120
	v_and_b32_e32 v118, 0xffff0000, v120
	v_lshlrev_b32_e32 v119, 16, v121
	v_and_b32_e32 v120, 0xffff0000, v121
	s_waitcnt vmcnt(19)
	v_lshlrev_b32_e32 v121, 16, v124
	v_and_b32_e32 v122, 0xffff0000, v124
	v_lshlrev_b32_e32 v123, 16, v125
	v_and_b32_e32 v124, 0xffff0000, v125
	s_waitcnt vmcnt(18)
	v_lshlrev_b32_e32 v125, 16, v128
	v_and_b32_e32 v126, 0xffff0000, v128
	v_lshlrev_b32_e32 v127, 16, v129
	v_and_b32_e32 v128, 0xffff0000, v129
	s_waitcnt vmcnt(17)
	v_lshlrev_b32_e32 v129, 16, v164
	v_and_b32_e32 v130, 0xffff0000, v164
	s_waitcnt vmcnt(16)
	v_lshlrev_b32_e32 v131, 16, v134
	v_and_b32_e32 v132, 0xffff0000, v134
	v_lshlrev_b32_e32 v133, 16, v135
	v_and_b32_e32 v134, 0xffff0000, v135
	s_waitcnt vmcnt(15)
	v_lshlrev_b32_e32 v135, 16, v138
	v_and_b32_e32 v136, 0xffff0000, v138
	v_lshlrev_b32_e32 v137, 16, v139
	v_and_b32_e32 v138, 0xffff0000, v139
	s_waitcnt vmcnt(14)
	v_lshlrev_b32_e32 v139, 16, v142
	v_and_b32_e32 v140, 0xffff0000, v142
	v_lshlrev_b32_e32 v141, 16, v143
	v_and_b32_e32 v142, 0xffff0000, v143
	s_waitcnt vmcnt(13)
	v_lshlrev_b32_e32 v143, 16, v146
	v_and_b32_e32 v144, 0xffff0000, v146
	v_lshlrev_b32_e32 v145, 16, v147
	v_and_b32_e32 v146, 0xffff0000, v147
	s_waitcnt vmcnt(12)
	v_lshlrev_b32_e32 v147, 16, v150
	v_and_b32_e32 v148, 0xffff0000, v150
	v_lshlrev_b32_e32 v149, 16, v151
	v_and_b32_e32 v150, 0xffff0000, v151
	s_waitcnt vmcnt(11)
	v_lshlrev_b32_e32 v151, 16, v154
	v_and_b32_e32 v152, 0xffff0000, v154
	v_lshlrev_b32_e32 v153, 16, v155
	v_and_b32_e32 v154, 0xffff0000, v155
	s_waitcnt vmcnt(10)
	v_lshlrev_b32_e32 v155, 16, v158
	v_and_b32_e32 v156, 0xffff0000, v158
	v_lshlrev_b32_e32 v157, 16, v159
	v_and_b32_e32 v158, 0xffff0000, v159
	s_waitcnt vmcnt(9)
	v_lshlrev_b32_e32 v159, 16, v162
	v_and_b32_e32 v160, 0xffff0000, v162
	v_lshlrev_b32_e32 v161, 16, v163
	v_and_b32_e32 v162, 0xffff0000, v163
	v_lshlrev_b32_e32 v163, 16, v165
	v_and_b32_e32 v164, 0xffff0000, v165
	s_waitcnt vmcnt(8)
	v_lshlrev_b32_e32 v165, 16, v168
	v_and_b32_e32 v166, 0xffff0000, v168
	v_lshlrev_b32_e32 v167, 16, v169
	v_and_b32_e32 v168, 0xffff0000, v169
.Lnb_no_next:
	s_add_u32 s18, s18, s6
	s_addc_u32 s19, s19, s7
	v_lshl_add_u64 v[36:37], v[36:37], 0, s[10:11]
	v_lshl_add_u64 v[38:39], v[38:39], 0, s[10:11]
	s_andn2_b64 vcc, exec, s[12:13]
	v_mov_b32_e32 v90, v105
	v_mov_b32_e32 v91, v106
	v_mov_b32_e32 v98, v107
	v_mov_b32_e32 v99, v108
	v_mov_b32_e32 v82, v109
	v_mov_b32_e32 v83, v110
	v_mov_b32_e32 v92, v111
	v_mov_b32_e32 v93, v112
	v_mov_b32_e32 v74, v113
	v_mov_b32_e32 v75, v114
	v_mov_b32_e32 v84, v115
	v_mov_b32_e32 v85, v116
	v_mov_b32_e32 v66, v117
	v_mov_b32_e32 v67, v118
	v_mov_b32_e32 v76, v119
	v_mov_b32_e32 v77, v120
	v_mov_b32_e32 v58, v121
	v_mov_b32_e32 v59, v122
	v_mov_b32_e32 v68, v123
	v_mov_b32_e32 v69, v124
	v_mov_b32_e32 v50, v125
	v_mov_b32_e32 v51, v126
	v_mov_b32_e32 v60, v127
	v_mov_b32_e32 v61, v128
	v_mov_b32_e32 v42, v129
	v_mov_b32_e32 v43, v130
	v_mov_b32_e32 v52, v163
	v_mov_b32_e32 v53, v164
	v_mov_b32_e32 v40, v165
	v_mov_b32_e32 v41, v166
	v_mov_b32_e32 v44, v167
	v_mov_b32_e32 v45, v168
	v_mov_b32_e32 v100, v131
	v_mov_b32_e32 v101, v132
	v_mov_b32_e32 v102, v133
	v_mov_b32_e32 v103, v134
	v_mov_b32_e32 v94, v135
	v_mov_b32_e32 v95, v136
	v_mov_b32_e32 v96, v137
	v_mov_b32_e32 v97, v138
	v_mov_b32_e32 v86, v139
	v_mov_b32_e32 v87, v140
	v_mov_b32_e32 v88, v141
	v_mov_b32_e32 v89, v142
	v_mov_b32_e32 v78, v143
	v_mov_b32_e32 v79, v144
	v_mov_b32_e32 v80, v145
	v_mov_b32_e32 v81, v146
	v_mov_b32_e32 v70, v147
	v_mov_b32_e32 v71, v148
	v_mov_b32_e32 v72, v149
	v_mov_b32_e32 v73, v150
	v_mov_b32_e32 v62, v151
	v_mov_b32_e32 v63, v152
	v_mov_b32_e32 v64, v153
	v_mov_b32_e32 v65, v154
	v_mov_b32_e32 v54, v155
	v_mov_b32_e32 v55, v156
	v_mov_b32_e32 v56, v157
	v_mov_b32_e32 v57, v158
	v_mov_b32_e32 v46, v159
	v_mov_b32_e32 v47, v160
	v_mov_b32_e32 v48, v161
	v_mov_b32_e32 v49, v162
	s_cbranch_vccz .LBB0_1631

.LBB0_1629:
	v_mul_f32_e32 v175, v101, v101
	v_mul_f32_e32 v170, v103, v103
	v_fmac_f32_e32 v175, v100, v100
	v_fmac_f32_e32 v170, v102, v102
	v_add_f32_e32 v175, v175, v170
	v_mul_f32_e32 v170, v95, v95
	v_mul_f32_e32 v171, v97, v97
	v_fmac_f32_e32 v170, v94, v94
	v_fmac_f32_e32 v171, v96, v96
	v_add_f32_e32 v170, v170, v171
	v_add_f32_e32 v175, v175, v170
	v_mul_f32_e32 v170, v87, v87
	v_mul_f32_e32 v171, v89, v89
	v_fmac_f32_e32 v170, v86, v86
	v_fmac_f32_e32 v171, v88, v88
	v_add_f32_e32 v170, v170, v171
	v_add_f32_e32 v175, v175, v170
	v_mul_f32_e32 v170, v79, v79
	v_mul_f32_e32 v171, v81, v81
	v_fmac_f32_e32 v170, v78, v78
	v_fmac_f32_e32 v171, v80, v80
	v_add_f32_e32 v170, v170, v171
	v_add_f32_e32 v175, v175, v170
	v_mul_f32_e32 v170, v71, v71
	v_mul_f32_e32 v171, v73, v73
	v_fmac_f32_e32 v170, v70, v70
	v_fmac_f32_e32 v171, v72, v72
	v_add_f32_e32 v170, v170, v171
	v_add_f32_e32 v175, v175, v170
	v_mul_f32_e32 v170, v63, v63
	v_mul_f32_e32 v171, v65, v65
	v_fmac_f32_e32 v170, v62, v62
	v_fmac_f32_e32 v171, v64, v64
	v_add_f32_e32 v170, v170, v171
	v_add_f32_e32 v175, v175, v170
	v_mul_f32_e32 v170, v55, v55
	v_mul_f32_e32 v171, v57, v57
	v_fmac_f32_e32 v170, v54, v54
	v_fmac_f32_e32 v171, v56, v56
	v_add_f32_e32 v170, v170, v171
	v_add_f32_e32 v175, v175, v170
	v_mul_f32_e32 v170, v47, v47
	v_mul_f32_e32 v171, v49, v49
	v_fmac_f32_e32 v170, v46, v46
	v_fmac_f32_e32 v171, v48, v48
	v_add_f32_e32 v170, v170, v171
	v_add_f32_e32 v175, v175, v170
	v_mov_b32_e32 v170, 0
	s_nop 0
	v_add_f32_dpp v175, v175, v175 quad_perm:[1,0,3,2] row_mask:0xf bank_mask:0xf bound_ctrl:1
	s_nop 1
	v_add_f32_dpp v175, v175, v175 quad_perm:[2,3,0,1] row_mask:0xf bank_mask:0xf bound_ctrl:1
	s_nop 1
	v_add_f32_dpp v175, v175, v175 row_half_mirror row_mask:0xf bank_mask:0xf bound_ctrl:1
	s_nop 1
	v_add_f32_dpp v175, v175, v175 row_mirror row_mask:0xf bank_mask:0xf bound_ctrl:1
	s_nop 1
	v_mov_b32_dpp v170, v175 row_bcast:15 row_mask:0xa bank_mask:0xf
	v_add_f32_e32 v175, v175, v170
	v_mov_b32_e32 v170, 0
	s_nop 1
	v_mov_b32_dpp v170, v175 row_bcast:31 row_mask:0xc bank_mask:0xf
	v_add_f32_e32 v175, v175, v170
	s_nop 0
	v_readlane_b32 s0, v175, 63
	s_nop 1
	v_fma_f32 v175, s0, v104, v1
	v_mul_f32_e32 v170, 0x4f800000, v175
	v_cmp_gt_f32_e32 vcc, s23, v175
	s_nop 1
	v_cndmask_b32_e32 v175, v175, v170, vcc
	v_sqrt_f32_e32 v170, v175
	s_nop 0
	v_add_u32_e32 v171, -1, v170
	v_fma_f32 v172, -v171, v170, v175
	v_cmp_ge_f32_e64 s[0:1], 0, v172
	v_add_u32_e32 v172, 1, v170
	s_nop 0
	v_cndmask_b32_e64 v171, v170, v171, s[0:1]
	v_fma_f32 v170, -v172, v170, v175
	v_cmp_lt_f32_e64 s[0:1], 0, v170
	s_nop 1
	v_cndmask_b32_e64 v170, v171, v172, s[0:1]
	v_mul_f32_e32 v171, 0x37800000, v170
	v_cndmask_b32_e32 v170, v170, v171, vcc
	v_cmp_class_f32_e32 vcc, v175, v34
	s_nop 1
	v_cndmask_b32_e32 v175, v170, v175, vcc
	v_div_scale_f32 v170, s[0:1], v175, v175, 1.0
	v_rcp_f32_e32 v171, v170
	s_nop 0
	v_fma_f32 v172, -v170, v171, 1.0
	v_fmac_f32_e32 v171, v172, v171
	v_div_scale_f32 v172, vcc, 1.0, v175, 1.0
	v_mul_f32_e32 v173, v172, v171
	v_fma_f32 v174, -v170, v173, v172
	v_fmac_f32_e32 v173, v174, v171
	v_fma_f32 v170, -v170, v173, v172
	v_div_fmas_f32 v170, v170, v171, v173
	v_div_fixup_f32 v170, v170, v175, 1.0
	v_pk_mul_f32 v[100:101], v[170:171], v[100:101] op_sel_hi:[0,1]
	v_pk_fma_f32 v[90:91], v[100:101], v[10:11], v[90:91]
	v_pk_mul_f32 v[48:49], v[170:171], v[48:49] op_sel_hi:[0,1]
	v_pk_fma_f32 v[44:45], v[48:49], v[32:33], v[44:45]
	v_bfe_u32 v48, v90, 16, 1
	v_pk_mul_f32 v[102:103], v[170:171], v[102:103] op_sel_hi:[0,1]
	v_add3_u32 v48, v90, v48, s16
	v_bfe_u32 v49, v91, 16, 1
	v_pk_fma_f32 v[98:99], v[102:103], v[12:13], v[98:99]
	v_lshrrev_b32_e32 v48, 16, v48
	v_add3_u32 v49, v91, v49, s16
	v_pk_mul_f32 v[54:55], v[170:171], v[54:55] op_sel_hi:[0,1]
	v_pk_mul_f32 v[46:47], v[170:171], v[46:47] op_sel_hi:[0,1]
	v_and_or_b32 v48, v49, s17, v48
	v_bfe_u32 v49, v98, 16, 1
	v_pk_fma_f32 v[42:43], v[54:55], v[26:27], v[42:43]
	v_pk_fma_f32 v[40:41], v[46:47], v[30:31], v[40:41]
	v_lshl_add_u64 v[46:47], s[86:87], 0, v[36:37]
	v_add3_u32 v49, v98, v49, s16
	v_bfe_u32 v54, v99, 16, 1
	v_pk_mul_f32 v[94:95], v[170:171], v[94:95] op_sel_hi:[0,1]
	v_lshrrev_b32_e32 v49, 16, v49
	v_add3_u32 v54, v99, v54, s16
	v_add_co_u32_e32 v46, vcc, s22, v46
	v_pk_fma_f32 v[82:83], v[94:95], v[2:3], v[82:83]
	v_and_or_b32 v49, v54, s17, v49
	v_addc_co_u32_e32 v47, vcc, 0, v47, vcc
	global_store_dwordx2 v[46:47], v[48:49], off
	v_bfe_u32 v48, v82, 16, 1
	v_pk_mul_f32 v[96:97], v[170:171], v[96:97] op_sel_hi:[0,1]
	v_add3_u32 v48, v82, v48, s16
	v_bfe_u32 v49, v83, 16, 1
	v_pk_fma_f32 v[92:93], v[96:97], v[4:5], v[92:93]
	v_lshrrev_b32_e32 v48, 16, v48
	v_add3_u32 v49, v83, v49, s16
	v_and_or_b32 v48, v49, s17, v48
	v_bfe_u32 v49, v92, 16, 1
	v_add3_u32 v49, v92, v49, s16
	v_bfe_u32 v54, v93, 16, 1
	v_pk_mul_f32 v[86:87], v[170:171], v[86:87] op_sel_hi:[0,1]
	v_lshrrev_b32_e32 v49, 16, v49
	v_add3_u32 v54, v93, v54, s16
	v_pk_fma_f32 v[74:75], v[86:87], v[6:7], v[74:75]
	v_and_or_b32 v49, v54, s17, v49
	global_store_dwordx2 v[46:47], v[48:49], off offset:512
	v_bfe_u32 v48, v74, 16, 1
	v_pk_mul_f32 v[88:89], v[170:171], v[88:89] op_sel_hi:[0,1]
	v_add3_u32 v48, v74, v48, s16
	v_bfe_u32 v49, v75, 16, 1
	v_pk_fma_f32 v[84:85], v[88:89], v[8:9], v[84:85]
	v_lshrrev_b32_e32 v48, 16, v48
	v_add3_u32 v49, v75, v49, s16
	v_and_or_b32 v48, v49, s17, v48
	v_bfe_u32 v49, v84, 16, 1
	v_add3_u32 v49, v84, v49, s16
	v_bfe_u32 v54, v85, 16, 1
	v_pk_mul_f32 v[78:79], v[170:171], v[78:79] op_sel_hi:[0,1]
	v_lshrrev_b32_e32 v49, 16, v49
	v_add3_u32 v54, v85, v54, s16
	v_pk_fma_f32 v[66:67], v[78:79], v[14:15], v[66:67]
	v_and_or_b32 v49, v54, s17, v49
	global_store_dwordx2 v[46:47], v[48:49], off offset:1024
	v_bfe_u32 v48, v66, 16, 1
	v_pk_mul_f32 v[80:81], v[170:171], v[80:81] op_sel_hi:[0,1]
	v_add3_u32 v48, v66, v48, s16
	v_bfe_u32 v49, v67, 16, 1
	v_pk_fma_f32 v[76:77], v[80:81], v[16:17], v[76:77]
	v_lshrrev_b32_e32 v48, 16, v48
	v_add3_u32 v49, v67, v49, s16
	v_and_or_b32 v48, v49, s17, v48
	v_bfe_u32 v49, v76, 16, 1
	v_add3_u32 v49, v76, v49, s16
	v_bfe_u32 v54, v77, 16, 1
	v_pk_mul_f32 v[70:71], v[170:171], v[70:71] op_sel_hi:[0,1]
	v_lshrrev_b32_e32 v49, 16, v49
	v_add3_u32 v54, v77, v54, s16
	v_pk_fma_f32 v[58:59], v[70:71], v[18:19], v[58:59]
	v_and_or_b32 v49, v54, s17, v49
	global_store_dwordx2 v[46:47], v[48:49], off offset:1536
	v_bfe_u32 v48, v58, 16, 1
	v_pk_mul_f32 v[72:73], v[170:171], v[72:73] op_sel_hi:[0,1]
	v_add3_u32 v48, v58, v48, s16
	v_bfe_u32 v49, v59, 16, 1
	v_pk_fma_f32 v[68:69], v[72:73], v[20:21], v[68:69]
	v_lshrrev_b32_e32 v48, 16, v48
	v_add3_u32 v49, v59, v49, s16
	v_and_or_b32 v48, v49, s17, v48
	v_bfe_u32 v49, v68, 16, 1
	v_add3_u32 v49, v68, v49, s16
	v_bfe_u32 v54, v69, 16, 1
	v_pk_mul_f32 v[62:63], v[170:171], v[62:63] op_sel_hi:[0,1]
	v_lshrrev_b32_e32 v49, 16, v49
	v_add3_u32 v54, v69, v54, s16
	v_pk_fma_f32 v[50:51], v[62:63], v[22:23], v[50:51]
	v_and_or_b32 v49, v54, s17, v49
	global_store_dwordx2 v[46:47], v[48:49], off offset:2048
	v_bfe_u32 v48, v50, 16, 1
	v_pk_mul_f32 v[64:65], v[170:171], v[64:65] op_sel_hi:[0,1]
	v_add3_u32 v48, v50, v48, s16
	v_bfe_u32 v49, v51, 16, 1
	v_pk_fma_f32 v[60:61], v[64:65], v[24:25], v[60:61]
	v_lshrrev_b32_e32 v48, 16, v48
	v_add3_u32 v49, v51, v49, s16
	v_and_or_b32 v48, v49, s17, v48
	v_bfe_u32 v49, v60, 16, 1
	v_add3_u32 v49, v60, v49, s16
	v_bfe_u32 v54, v61, 16, 1
	v_lshrrev_b32_e32 v49, 16, v49
	v_add3_u32 v54, v61, v54, s16
	v_and_or_b32 v49, v54, s17, v49
	global_store_dwordx2 v[46:47], v[48:49], off offset:2560
	v_bfe_u32 v48, v42, 16, 1
	v_pk_mul_f32 v[56:57], v[170:171], v[56:57] op_sel_hi:[0,1]
	v_add3_u32 v48, v42, v48, s16
	v_bfe_u32 v49, v43, 16, 1
	v_pk_fma_f32 v[52:53], v[56:57], v[28:29], v[52:53]
	v_lshrrev_b32_e32 v48, 16, v48
	v_add3_u32 v49, v43, v49, s16
	v_and_or_b32 v48, v49, s17, v48
	v_bfe_u32 v49, v52, 16, 1
	v_add3_u32 v49, v52, v49, s16
	v_bfe_u32 v54, v53, 16, 1
	v_lshrrev_b32_e32 v49, 16, v49
	v_add3_u32 v54, v53, v54, s16
	v_and_or_b32 v49, v54, s17, v49
	global_store_dwordx2 v[46:47], v[48:49], off offset:3072
	v_bfe_u32 v48, v40, 16, 1
	v_add3_u32 v48, v40, v48, s16
	v_bfe_u32 v49, v41, 16, 1
	v_lshrrev_b32_e32 v48, 16, v48
	v_add3_u32 v49, v41, v49, s16
	v_and_or_b32 v48, v49, s17, v48
	v_bfe_u32 v49, v44, 16, 1
	v_add3_u32 v49, v44, v49, s16
	v_bfe_u32 v54, v45, 16, 1
	v_lshrrev_b32_e32 v49, 16, v49
	v_add3_u32 v54, v45, v54, s16
	v_and_or_b32 v49, v54, s17, v49
	global_store_dwordx2 v[46:47], v[48:49], off offset:3584
	v_mul_f32_e32 v46, v91, v91
	v_mul_f32_e32 v47, v99, v99
	v_fmac_f32_e32 v46, v90, v90
	v_fmac_f32_e32 v47, v98, v98
	v_add_f32_e32 v46, v46, v47
	v_mul_f32_e32 v47, v83, v83
	v_mul_f32_e32 v48, v93, v93
	v_fmac_f32_e32 v47, v82, v82
	v_fmac_f32_e32 v48, v92, v92
	v_add_f32_e32 v47, v47, v48
	v_add_f32_e32 v46, v46, v47
	v_mul_f32_e32 v47, v75, v75
	v_mul_f32_e32 v48, v85, v85
	v_fmac_f32_e32 v47, v74, v74
	v_fmac_f32_e32 v48, v84, v84
	v_add_f32_e32 v47, v47, v48
	v_add_f32_e32 v46, v46, v47
	v_mul_f32_e32 v47, v67, v67
	v_mul_f32_e32 v48, v77, v77
	v_fmac_f32_e32 v47, v66, v66
	v_fmac_f32_e32 v48, v76, v76
	v_add_f32_e32 v47, v47, v48
	v_add_f32_e32 v46, v46, v47
	v_mul_f32_e32 v47, v59, v59
	v_mul_f32_e32 v48, v69, v69
	v_fmac_f32_e32 v47, v58, v58
	v_fmac_f32_e32 v48, v68, v68
	v_add_f32_e32 v47, v47, v48
	v_add_f32_e32 v46, v46, v47
	v_mul_f32_e32 v47, v51, v51
	v_mul_f32_e32 v48, v61, v61
	v_mul_f32_e32 v43, v43, v43
	v_fmac_f32_e32 v47, v50, v50
	v_fmac_f32_e32 v48, v60, v60
	v_fmac_f32_e32 v43, v42, v42
	v_mul_f32_e32 v42, v53, v53
	v_mul_f32_e32 v41, v41, v41
	v_add_f32_e32 v47, v47, v48
	v_fmac_f32_e32 v42, v52, v52
	v_fmac_f32_e32 v41, v40, v40
	v_mul_f32_e32 v40, v45, v45
	v_add_f32_e32 v46, v46, v47
	v_add_f32_e32 v42, v43, v42
	v_fmac_f32_e32 v40, v44, v44
	v_add_f32_e32 v42, v46, v42
	v_add_f32_e32 v40, v41, v40
	v_add_f32_e32 v40, v42, v40
	v_mov_b32_e32 v41, 0
	s_nop 0
	v_add_f32_dpp v40, v40, v40 quad_perm:[1,0,3,2] row_mask:0xf bank_mask:0xf bound_ctrl:1
	s_nop 1
	v_add_f32_dpp v40, v40, v40 quad_perm:[2,3,0,1] row_mask:0xf bank_mask:0xf bound_ctrl:1
	s_nop 1
	v_add_f32_dpp v40, v40, v40 row_half_mirror row_mask:0xf bank_mask:0xf bound_ctrl:1
	s_nop 1
	v_add_f32_dpp v40, v40, v40 row_mirror row_mask:0xf bank_mask:0xf bound_ctrl:1
	s_nop 1
	v_mov_b32_dpp v41, v40 row_bcast:15 row_mask:0xa bank_mask:0xf
	v_add_f32_e32 v40, v40, v41
	v_mov_b32_e32 v41, 0
	s_nop 1
	v_mov_b32_dpp v41, v40 row_bcast:31 row_mask:0xc bank_mask:0xf
	v_add_f32_e32 v40, v40, v41
	s_nop 0
	v_readlane_b32 s0, v40, 63
	s_and_saveexec_b64 s[14:15], s[8:9]
	s_cbranch_execz .LBB0_1626
	v_fma_f32 v40, s0, v104, v1
	v_mul_f32_e32 v41, 0x4f800000, v40
	v_cmp_gt_f32_e32 vcc, s23, v40
	s_nop 1
	v_cndmask_b32_e32 v40, v40, v41, vcc
	v_sqrt_f32_e32 v41, v40
	s_nop 0
	v_add_u32_e32 v42, -1, v41
	v_fma_f32 v44, -v42, v41, v40
	v_add_u32_e32 v43, 1, v41
	v_cmp_ge_f32_e64 s[0:1], 0, v44
	s_nop 1
	v_cndmask_b32_e64 v42, v41, v42, s[0:1]
	v_fma_f32 v41, -v43, v41, v40
	v_cmp_lt_f32_e64 s[0:1], 0, v41
	s_nop 1
	v_cndmask_b32_e64 v41, v42, v43, s[0:1]
	v_mul_f32_e32 v42, 0x37800000, v41
	v_cndmask_b32_e32 v41, v41, v42, vcc
	v_cmp_class_f32_e32 vcc, v40, v34
	s_nop 1
	v_cndmask_b32_e32 v40, v41, v40, vcc
	v_div_scale_f32 v41, s[0:1], v40, v40, 1.0
	v_rcp_f32_e32 v42, v41
	s_add_u32 s0, s86, s18
	s_addc_u32 s1, s87, s19
	v_fma_f32 v43, -v41, v42, 1.0
	v_fmac_f32_e32 v42, v43, v42
	v_div_scale_f32 v43, vcc, 1.0, v40, 1.0
	v_mul_f32_e32 v44, v43, v42
	v_fma_f32 v45, -v41, v44, v43
	v_fmac_f32_e32 v44, v45, v42
	v_fma_f32 v41, -v41, v44, v43
	v_div_fmas_f32 v41, v41, v42, v44
	v_div_fixup_f32 v40, v41, v40, 1.0
	global_store_dword v35, v40, s[0:1]
	s_branch .LBB0_1626

.LBB0_2184:
	s_or_b64 exec, exec, s[4:5]
	s_cmp_lt_i32 s84, 0x8000
	s_waitcnt lgkmcnt(0)
	s_barrier
	s_cbranch_scc0 .LBB0_2195
	v_lshlrev_b32_e32 v66, 4, v236
	v_mov_b32_e32 v67, 0
	v_lshl_add_u64 v[50:51], s[90:91], 0, v[66:67]
	v_add_co_u32_e32 v28, vcc, 0xa000, v50
	s_ashr_i32 s85, s84, 31
	s_nop 0
	v_addc_co_u32_e32 v29, vcc, 0, v51, vcc
	v_add_co_u32_e32 v42, vcc, 0xb000, v50
	s_lshl_b64 s[6:7], s[84:85], 11
	s_lshl_b64 s[0:1], s[84:85], 12
	v_addc_co_u32_e32 v43, vcc, 0, v51, vcc
	s_add_u32 s4, s2, s0
	v_add_co_u32_e32 v54, vcc, 0xc000, v50
	s_addc_u32 s5, s3, s1
	v_lshlrev_b32_e32 v74, 3, v236
	v_addc_co_u32_e32 v55, vcc, 0, v51, vcc
	global_load_dwordx2 v[68:69], v74, s[4:5] nt
	global_load_dwordx2 v[70:71], v74, s[4:5] offset:512 nt
	global_load_dwordx2 v[72:73], v74, s[4:5] offset:1024 nt
	global_load_dwordx2 v[76:77], v74, s[4:5] offset:1536 nt
	global_load_dwordx2 v[78:79], v74, s[4:5] offset:2048 nt
	global_load_dwordx2 v[80:81], v74, s[4:5] offset:2560 nt
	global_load_dwordx2 v[82:83], v74, s[4:5] offset:3072 nt
	global_load_dwordx2 v[92:93], v74, s[4:5] offset:3584 nt
	s_mov_b64 s[8:9], 0xa000
	s_mov_b64 s[10:11], 0xc000
	s_add_u32 s4, s20, s0
	v_add_co_u32_e32 v84, vcc, 0xd000, v50
	s_addc_u32 s5, s21, s1
	v_lshl_add_u64 v[26:27], v[50:51], 0, s[8:9]
	v_lshl_add_u64 v[52:53], v[50:51], 0, s[10:11]
	v_addc_co_u32_e32 v85, vcc, 0, v51, vcc
	global_load_dwordx2 v[98:99], v74, s[4:5] nt
	global_load_dwordx2 v[100:101], v74, s[4:5] offset:512 nt
	global_load_dwordx2 v[106:107], v74, s[4:5] offset:1024 nt
	global_load_dwordx2 v[108:109], v74, s[4:5] offset:1536 nt
	global_load_dwordx4 v[2:5], v[26:27], off offset:1024
	global_load_dwordx4 v[6:9], v[26:27], off offset:2048
	global_load_dwordx2 v[114:115], v74, s[4:5] offset:2048 nt
	global_load_dwordx4 v[10:13], v[52:53], off offset:1024
	global_load_dwordx4 v[14:17], v[52:53], off offset:2048
	global_load_dwordx2 v[140:141], v74, s[4:5] offset:2560 nt
	global_load_dwordx4 v[18:21], v[28:29], off
	global_load_dwordx4 v[22:25], v[26:27], off offset:3072
	global_load_dwordx2 v[142:143], v74, s[4:5] offset:3072 nt
	global_load_dwordx2 v[144:145], v74, s[4:5] offset:3584 nt
	s_nop 0
	global_load_dwordx4 v[26:29], v[42:43], off
	global_load_dwordx4 v[30:33], v[42:43], off offset:1024
	global_load_dwordx4 v[34:37], v[42:43], off offset:2048
	global_load_dwordx4 v[38:41], v[42:43], off offset:3072
	s_nop 0
	global_load_dwordx4 v[42:45], v[54:55], off
	global_load_dwordx4 v[46:49], v[52:53], off offset:3072
	s_nop 0
	global_load_dwordx4 v[50:53], v[84:85], off
	global_load_dwordx4 v[54:57], v[84:85], off offset:1024
	global_load_dwordx4 v[58:61], v[84:85], off offset:2048
	global_load_dwordx4 v[62:65], v[84:85], off offset:3072
	v_mov_b32_e32 v75, v67
	s_mov_b32 s33, 0xffff0000
	v_add_u32_e32 v1, 0, v66
	v_cmp_eq_u32_e64 s[4:5], 0, v236
	s_movk_i32 s44, 0x7fff
	v_mov_b32_e32 v66, 0x358637bd
	s_mov_b32 s45, 0xf800000
	s_mov_b32 s46, 0x5b200000
	s_mov_b32 s47, 0xc3e00000
	s_mov_b32 s48, 0x1d800000
	s_mov_b32 s49, 0x3fb8aa3b
	s_mov_b32 s50, 0xc2ce8ed0
	s_mov_b32 s51, 0x42b17218
	s_mov_b32 s34, s84
	s_waitcnt vmcnt(31)
	v_lshlrev_b32_e32 v118, 16, v68
	v_and_b32_e32 v119, 0xffff0000, v68
	v_lshlrev_b32_e32 v120, 16, v69
	v_and_b32_e32 v121, 0xffff0000, v69
	v_lshl_add_u64 v[68:69], s[2:3], 0, v[74:75]
	s_lshl_b64 s[2:3], s[84:85], 2
	s_add_u32 s42, s2, 0x200000
	s_addc_u32 s43, s3, 0
	s_ashr_i32 s67, s66, 31
	s_waitcnt vmcnt(30)
	v_lshlrev_b32_e32 v110, 16, v70
	v_and_b32_e32 v111, 0xffff0000, v70
	v_lshlrev_b32_e32 v112, 16, v71
	v_and_b32_e32 v113, 0xffff0000, v71
	s_waitcnt vmcnt(29)
	v_lshlrev_b32_e32 v102, 16, v72
	v_and_b32_e32 v103, 0xffff0000, v72
	v_lshlrev_b32_e32 v104, 16, v73
	v_and_b32_e32 v105, 0xffff0000, v73
	s_waitcnt vmcnt(28)
	v_lshlrev_b32_e32 v94, 16, v76
	v_and_b32_e32 v95, 0xffff0000, v76
	v_lshlrev_b32_e32 v96, 16, v77
	v_and_b32_e32 v97, 0xffff0000, v77
	s_waitcnt vmcnt(27)
	v_lshlrev_b32_e32 v88, 16, v78
	v_and_b32_e32 v89, 0xffff0000, v78
	v_lshlrev_b32_e32 v90, 16, v79
	v_and_b32_e32 v91, 0xffff0000, v79
	s_waitcnt vmcnt(26)
	v_lshlrev_b32_e32 v84, 16, v80
	v_and_b32_e32 v85, 0xffff0000, v80
	v_lshlrev_b32_e32 v86, 16, v81
	v_and_b32_e32 v87, 0xffff0000, v81
	s_waitcnt vmcnt(25)
	v_lshlrev_b32_e32 v80, 16, v82
	v_and_b32_e32 v81, 0xffff0000, v82
	v_lshlrev_b32_e32 v82, 16, v83
	v_and_b32_e32 v83, 0xffff0000, v83
	s_waitcnt vmcnt(24)
	v_lshlrev_b32_e32 v76, 16, v92
	v_and_b32_e32 v77, 0xffff0000, v92
	v_lshlrev_b32_e32 v78, 16, v93
	v_and_b32_e32 v79, 0xffff0000, v93
	s_waitcnt vmcnt(23)
	v_lshlrev_b32_e32 v136, 16, v98
	v_and_b32_e32 v137, 0xffff0000, v98
	v_lshlrev_b32_e32 v138, 16, v99
	v_and_b32_e32 v139, 0xffff0000, v99
	s_waitcnt vmcnt(22)
	v_lshlrev_b32_e32 v132, 16, v100
	v_and_b32_e32 v133, 0xffff0000, v100
	v_lshlrev_b32_e32 v134, 16, v101
	v_and_b32_e32 v135, 0xffff0000, v101
	s_waitcnt vmcnt(21)
	v_lshlrev_b32_e32 v128, 16, v106
	v_and_b32_e32 v129, 0xffff0000, v106
	v_lshlrev_b32_e32 v130, 16, v107
	v_and_b32_e32 v131, 0xffff0000, v107
	s_waitcnt vmcnt(20)
	v_lshlrev_b32_e32 v124, 16, v108
	v_and_b32_e32 v125, 0xffff0000, v108
	v_lshlrev_b32_e32 v126, 16, v109
	v_and_b32_e32 v127, 0xffff0000, v109
	s_waitcnt vmcnt(17)
	v_lshlrev_b32_e32 v116, 16, v114
	v_and_b32_e32 v117, 0xffff0000, v114
	v_lshlrev_b32_e32 v122, 16, v115
	v_and_b32_e32 v123, 0xffff0000, v115
	s_waitcnt vmcnt(14)
	v_lshlrev_b32_e32 v108, 16, v140
	v_and_b32_e32 v109, 0xffff0000, v140
	v_lshlrev_b32_e32 v114, 16, v141
	v_and_b32_e32 v115, 0xffff0000, v141
	s_waitcnt vmcnt(11)
	v_lshlrev_b32_e32 v100, 16, v142
	v_and_b32_e32 v101, 0xffff0000, v142
	v_lshlrev_b32_e32 v106, 16, v143
	v_and_b32_e32 v107, 0xffff0000, v143
	s_waitcnt vmcnt(10)
	v_lshlrev_b32_e32 v92, 16, v144
	v_and_b32_e32 v93, 0xffff0000, v144
	v_lshlrev_b32_e32 v98, 16, v145
	v_and_b32_e32 v99, 0xffff0000, v145
	v_lshl_add_u64 v[70:71], s[20:21], 0, v[74:75]
	s_lshl_b64 s[22:23], s[66:67], 2
	s_lshl_b64 s[24:25], s[84:85], 3
	s_lshl_b64 s[26:27], s[66:67], 3
	v_lshl_or_b32 v72, v236, 2, s6
	v_mov_b32_e32 v73, s7
	s_lshl_b64 s[28:29], s[66:67], 11
	v_or_b32_e32 v74, s0, v74
	v_mov_b32_e32 v75, s1
	s_lshl_b64 s[30:31], s[66:67], 12
	v_mov_b32_e32 v140, 0x260
	v_mov_b32_e32 v141, 0x220000
	v_mov_b32_e32 v142, 0x3a000000
	v_mov_b32_e32 v143, 0x43e00000
	v_mov_b32_e32 v144, 0xff800000
	v_mov_b32_e32 v145, 0x7f800000
	s_waitcnt vmcnt(0)
	s_branch .LBB0_2188

.LBB0_2187:
	s_or_b64 exec, exec, s[38:39]
	s_and_b64 vcc, exec, s[36:37]
	s_cbranch_vccnz .Lnc_no_next
	s_waitcnt vmcnt(31)
	v_lshlrev_b32_e32 v158, 16, v148
	v_and_b32_e32 v159, 0xffff0000, v148
	v_lshlrev_b32_e32 v160, 16, v149
	v_and_b32_e32 v161, 0xffff0000, v149
	s_waitcnt vmcnt(30)
	v_lshlrev_b32_e32 v166, 16, v150
	v_and_b32_e32 v167, 0xffff0000, v150
	v_lshlrev_b32_e32 v168, 16, v151
	v_and_b32_e32 v169, 0xffff0000, v151
	s_waitcnt vmcnt(29)
	v_lshlrev_b32_e32 v174, 16, v152
	v_and_b32_e32 v175, 0xffff0000, v152
	v_lshlrev_b32_e32 v176, 16, v153
	v_and_b32_e32 v177, 0xffff0000, v153
	s_waitcnt vmcnt(28)
	v_lshlrev_b32_e32 v182, 16, v154
	v_and_b32_e32 v183, 0xffff0000, v154
	v_lshlrev_b32_e32 v184, 16, v155
	v_and_b32_e32 v185, 0xffff0000, v155
	s_waitcnt vmcnt(27)
	v_lshlrev_b32_e32 v190, 16, v156
	v_and_b32_e32 v191, 0xffff0000, v156
	v_lshlrev_b32_e32 v192, 16, v157
	v_and_b32_e32 v193, 0xffff0000, v157
	s_waitcnt vmcnt(26)
	v_lshlrev_b32_e32 v198, 16, v162
	v_and_b32_e32 v199, 0xffff0000, v162
	v_lshlrev_b32_e32 v200, 16, v163
	v_and_b32_e32 v201, 0xffff0000, v163
	s_waitcnt vmcnt(25)
	v_lshlrev_b32_e32 v202, 16, v164
	v_and_b32_e32 v203, 0xffff0000, v164
	v_lshlrev_b32_e32 v204, 16, v165
	v_and_b32_e32 v205, 0xffff0000, v165
	s_waitcnt vmcnt(24)
	v_lshlrev_b32_e32 v206, 16, v146
	v_and_b32_e32 v207, 0xffff0000, v146
	v_lshlrev_b32_e32 v208, 16, v147
	v_and_b32_e32 v209, 0xffff0000, v147
	s_waitcnt vmcnt(23)
	v_lshlrev_b32_e32 v146, 16, v170
	v_and_b32_e32 v147, 0xffff0000, v170
	v_lshlrev_b32_e32 v148, 16, v171
	v_and_b32_e32 v149, 0xffff0000, v171
	s_waitcnt vmcnt(22)
	v_lshlrev_b32_e32 v150, 16, v172
	v_and_b32_e32 v151, 0xffff0000, v172
	v_lshlrev_b32_e32 v152, 16, v173
	v_and_b32_e32 v153, 0xffff0000, v173
	s_waitcnt vmcnt(21)
	v_lshlrev_b32_e32 v154, 16, v178
	v_and_b32_e32 v155, 0xffff0000, v178
	v_lshlrev_b32_e32 v156, 16, v179
	v_and_b32_e32 v157, 0xffff0000, v179
	s_waitcnt vmcnt(20)
	v_lshlrev_b32_e32 v162, 16, v180
	v_and_b32_e32 v163, 0xffff0000, v180
	v_lshlrev_b32_e32 v164, 16, v181
	v_and_b32_e32 v165, 0xffff0000, v181
	s_waitcnt vmcnt(19)
	v_lshlrev_b32_e32 v170, 16, v186
	v_and_b32_e32 v171, 0xffff0000, v186
	v_lshlrev_b32_e32 v172, 16, v187
	v_and_b32_e32 v173, 0xffff0000, v187
	s_waitcnt vmcnt(18)
	v_lshlrev_b32_e32 v178, 16, v188
	v_and_b32_e32 v179, 0xffff0000, v188
	v_lshlrev_b32_e32 v180, 16, v189
	v_and_b32_e32 v181, 0xffff0000, v189
	s_waitcnt vmcnt(17)
	v_lshlrev_b32_e32 v186, 16, v194
	v_and_b32_e32 v187, 0xffff0000, v194
	v_lshlrev_b32_e32 v188, 16, v195
	v_and_b32_e32 v189, 0xffff0000, v195
	s_waitcnt vmcnt(16)
	v_lshlrev_b32_e32 v194, 16, v196
	v_and_b32_e32 v195, 0xffff0000, v196
	v_lshlrev_b32_e32 v196, 16, v197
	v_and_b32_e32 v197, 0xffff0000, v197
.Lnc_no_next:
	s_add_u32 s42, s42, s22
	s_addc_u32 s43, s43, s23
	s_add_u32 s24, s24, s26
	s_addc_u32 s25, s25, s27
	v_lshl_add_u64 v[72:73], v[72:73], 0, s[28:29]
	v_lshl_add_u64 v[74:75], v[74:75], 0, s[30:31]
	s_andn2_b64 vcc, exec, s[36:37]
	v_mov_b32_e32 v76, v206
	v_mov_b32_e32 v77, v207
	v_mov_b32_e32 v78, v208
	v_mov_b32_e32 v79, v209
	v_mov_b32_e32 v80, v202
	v_mov_b32_e32 v81, v203
	v_mov_b32_e32 v82, v204
	v_mov_b32_e32 v83, v205
	v_mov_b32_e32 v84, v198
	v_mov_b32_e32 v85, v199
	v_mov_b32_e32 v86, v200
	v_mov_b32_e32 v87, v201
	v_mov_b32_e32 v88, v190
	v_mov_b32_e32 v89, v191
	v_mov_b32_e32 v90, v192
	v_mov_b32_e32 v91, v193
	v_mov_b32_e32 v94, v182
	v_mov_b32_e32 v95, v183
	v_mov_b32_e32 v96, v184
	v_mov_b32_e32 v97, v185
	v_mov_b32_e32 v102, v174
	v_mov_b32_e32 v103, v175
	v_mov_b32_e32 v104, v176
	v_mov_b32_e32 v105, v177
	v_mov_b32_e32 v110, v166
	v_mov_b32_e32 v111, v167
	v_mov_b32_e32 v112, v168
	v_mov_b32_e32 v113, v169
	v_mov_b32_e32 v118, v158
	v_mov_b32_e32 v119, v159
	v_mov_b32_e32 v120, v160
	v_mov_b32_e32 v121, v161
	v_mov_b32_e32 v92, v194
	v_mov_b32_e32 v93, v195
	v_mov_b32_e32 v98, v196
	v_mov_b32_e32 v99, v197
	v_mov_b32_e32 v100, v186
	v_mov_b32_e32 v101, v187
	v_mov_b32_e32 v106, v188
	v_mov_b32_e32 v107, v189
	v_mov_b32_e32 v108, v178
	v_mov_b32_e32 v109, v179
	v_mov_b32_e32 v114, v180
	v_mov_b32_e32 v115, v181
	v_mov_b32_e32 v116, v170
	v_mov_b32_e32 v117, v171
	v_mov_b32_e32 v122, v172
	v_mov_b32_e32 v123, v173
	v_mov_b32_e32 v124, v162
	v_mov_b32_e32 v125, v163
	v_mov_b32_e32 v126, v164
	v_mov_b32_e32 v127, v165
	v_mov_b32_e32 v128, v154
	v_mov_b32_e32 v129, v155
	v_mov_b32_e32 v130, v156
	v_mov_b32_e32 v131, v157
	v_mov_b32_e32 v132, v150
	v_mov_b32_e32 v133, v151
	v_mov_b32_e32 v134, v152
	v_mov_b32_e32 v135, v153
	v_mov_b32_e32 v136, v146
	v_mov_b32_e32 v137, v147
	v_mov_b32_e32 v138, v148
	v_mov_b32_e32 v139, v149
	s_cbranch_vccz .LBB0_2195

.LBB0_2190:
	v_mul_f32_e32 v210, v119, v119
	v_mul_f32_e32 v211, v121, v121
	v_fmac_f32_e32 v210, v118, v118
	v_fmac_f32_e32 v211, v120, v120
	v_add_f32_e32 v210, v210, v211
	v_mul_f32_e32 v211, v111, v111
	v_mul_f32_e32 v212, v113, v113
	v_fmac_f32_e32 v211, v110, v110
	v_fmac_f32_e32 v212, v112, v112
	v_add_f32_e32 v211, v211, v212
	v_add_f32_e32 v210, v210, v211
	v_mul_f32_e32 v211, v103, v103
	v_mul_f32_e32 v212, v105, v105
	v_fmac_f32_e32 v211, v102, v102
	v_fmac_f32_e32 v212, v104, v104
	v_add_f32_e32 v211, v211, v212
	v_add_f32_e32 v210, v210, v211
	v_mul_f32_e32 v211, v95, v95
	v_mul_f32_e32 v212, v97, v97
	v_fmac_f32_e32 v211, v94, v94
	v_fmac_f32_e32 v212, v96, v96
	v_add_f32_e32 v211, v211, v212
	v_add_f32_e32 v210, v210, v211
	v_mul_f32_e32 v211, v89, v89
	v_mul_f32_e32 v212, v91, v91
	v_fmac_f32_e32 v211, v88, v88
	v_fmac_f32_e32 v212, v90, v90
	v_add_f32_e32 v211, v211, v212
	v_add_f32_e32 v210, v210, v211
	v_mul_f32_e32 v211, v85, v85
	v_mul_f32_e32 v212, v87, v87
	v_fmac_f32_e32 v211, v84, v84
	v_fmac_f32_e32 v212, v86, v86
	v_add_f32_e32 v211, v211, v212
	v_add_f32_e32 v210, v210, v211
	v_mul_f32_e32 v211, v81, v81
	v_mul_f32_e32 v212, v83, v83
	v_fmac_f32_e32 v211, v80, v80
	v_fmac_f32_e32 v212, v82, v82
	v_add_f32_e32 v211, v211, v212
	v_add_f32_e32 v210, v210, v211
	v_mul_f32_e32 v211, v77, v77
	v_mul_f32_e32 v212, v79, v79
	v_fmac_f32_e32 v211, v76, v76
	v_fmac_f32_e32 v212, v78, v78
	v_add_f32_e32 v211, v211, v212
	v_add_f32_e32 v210, v210, v211
	v_mov_b32_e32 v211, 0
	s_nop 0
	v_add_f32_dpp v210, v210, v210 quad_perm:[1,0,3,2] row_mask:0xf bank_mask:0xf bound_ctrl:1
	s_nop 1
	v_add_f32_dpp v210, v210, v210 quad_perm:[2,3,0,1] row_mask:0xf bank_mask:0xf bound_ctrl:1
	s_nop 1
	v_add_f32_dpp v210, v210, v210 row_half_mirror row_mask:0xf bank_mask:0xf bound_ctrl:1
	s_nop 1
	v_add_f32_dpp v210, v210, v210 row_mirror row_mask:0xf bank_mask:0xf bound_ctrl:1
	s_nop 1
	v_mov_b32_dpp v211, v210 row_bcast:15 row_mask:0xa bank_mask:0xf
	v_add_f32_e32 v210, v210, v211
	v_mov_b32_e32 v211, 0
	s_nop 1
	v_mov_b32_dpp v211, v210 row_bcast:31 row_mask:0xc bank_mask:0xf
	v_add_f32_e32 v210, v210, v211
	s_nop 0
	v_readlane_b32 s0, v210, 63
	s_nop 1
	v_fma_f32 v210, s0, v142, v66
	v_mul_f32_e32 v211, 0x4f800000, v210
	v_cmp_gt_f32_e32 vcc, s45, v210
	s_nop 1
	v_cndmask_b32_e32 v210, v210, v211, vcc
	v_sqrt_f32_e32 v211, v210
	s_nop 0
	v_add_u32_e32 v212, -1, v211
	v_fma_f32 v213, -v212, v211, v210
	v_cmp_ge_f32_e64 s[0:1], 0, v213
	v_add_u32_e32 v213, 1, v211
	s_nop 0
	v_cndmask_b32_e64 v212, v211, v212, s[0:1]
	v_fma_f32 v211, -v213, v211, v210
	v_cmp_lt_f32_e64 s[0:1], 0, v211
	s_nop 1
	v_cndmask_b32_e64 v211, v212, v213, s[0:1]
	v_mul_f32_e32 v212, 0x37800000, v211
	v_cndmask_b32_e32 v211, v211, v212, vcc
	v_cmp_class_f32_e32 vcc, v210, v140
	s_nop 1
	v_cndmask_b32_e32 v210, v211, v210, vcc
	v_div_scale_f32 v211, s[0:1], v210, v210, 1.0
	v_rcp_f32_e32 v212, v211
	s_nop 0
	v_fma_f32 v213, -v211, v212, 1.0
	v_fmac_f32_e32 v212, v213, v212
	v_div_scale_f32 v213, vcc, 1.0, v210, 1.0
	v_mul_f32_e32 v214, v213, v212
	v_fma_f32 v215, -v211, v214, v213
	v_fmac_f32_e32 v214, v215, v212
	v_fma_f32 v211, -v211, v214, v213
	v_div_fmas_f32 v211, v211, v212, v214
	v_div_fixup_f32 v210, v211, v210, 1.0
	v_pk_mul_f32 v[94:95], v[210:211], v[94:95] op_sel_hi:[0,1]
	v_pk_fma_f32 v[124:125], v[94:95], v[22:23], v[124:125]
	v_pk_mul_f32 v[94:95], v[210:211], v[88:89] op_sel_hi:[0,1]
	v_pk_mul_f32 v[212:213], v[210:211], v[118:119] op_sel_hi:[0,1]
	v_pk_mul_f32 v[88:89], v[210:211], v[90:91] op_sel_hi:[0,1]
	v_pk_fma_f32 v[90:91], v[94:95], v[26:27], v[116:117]
	v_pk_mul_f32 v[94:95], v[210:211], v[84:85] op_sel_hi:[0,1]
	v_pk_mul_f32 v[84:85], v[210:211], v[86:87] op_sel_hi:[0,1]
	v_pk_mul_f32 v[86:87], v[210:211], v[80:81] op_sel_hi:[0,1]
	v_pk_mul_f32 v[118:119], v[210:211], v[120:121] op_sel_hi:[0,1]
	v_pk_fma_f32 v[120:121], v[212:213], v[18:19], v[136:137]
	v_pk_mul_f32 v[80:81], v[210:211], v[82:83] op_sel_hi:[0,1]
	v_pk_fma_f32 v[82:83], v[86:87], v[34:35], v[100:101]
	v_pk_mul_f32 v[86:87], v[210:211], v[76:77] op_sel_hi:[0,1]
	v_pk_fma_f32 v[84:85], v[84:85], v[32:33], v[114:115]
	v_pk_fma_f32 v[114:115], v[86:87], v[38:39], v[92:93]
	v_bfe_u32 v86, v120, 16, 1
	v_add3_u32 v86, v120, v86, s44
	v_bfe_u32 v87, v121, 16, 1
	v_pk_fma_f32 v[118:119], v[118:119], v[20:21], v[138:139]
	v_lshrrev_b32_e32 v86, 16, v86
	v_add3_u32 v87, v121, v87, s44
	v_and_or_b32 v86, v87, s33, v86
	v_bfe_u32 v87, v118, 16, 1
	v_pk_mul_f32 v[76:77], v[210:211], v[78:79] op_sel_hi:[0,1]
	v_lshl_add_u64 v[78:79], s[86:87], 0, v[74:75]
	v_add3_u32 v87, v118, v87, s44
	v_bfe_u32 v92, v119, 16, 1
	v_pk_mul_f32 v[136:137], v[210:211], v[110:111] op_sel_hi:[0,1]
	v_lshrrev_b32_e32 v87, 16, v87
	v_add3_u32 v92, v119, v92, s44
	v_add_co_u32_e32 v78, vcc, s46, v78
	v_pk_mul_f32 v[110:111], v[210:211], v[112:113] op_sel_hi:[0,1]
	v_pk_fma_f32 v[112:113], v[136:137], v[2:3], v[132:133]
	v_and_or_b32 v87, v92, s33, v87
	v_addc_co_u32_e32 v79, vcc, 0, v79, vcc
	global_store_dwordx2 v[78:79], v[86:87], off nt
	v_bfe_u32 v86, v112, 16, 1
	v_add3_u32 v86, v112, v86, s44
	v_bfe_u32 v87, v113, 16, 1
	v_pk_fma_f32 v[110:111], v[110:111], v[4:5], v[134:135]
	v_lshrrev_b32_e32 v86, 16, v86
	v_add3_u32 v87, v113, v87, s44
	v_and_or_b32 v86, v87, s33, v86
	v_bfe_u32 v87, v110, 16, 1
	v_add3_u32 v87, v110, v87, s44
	v_bfe_u32 v92, v111, 16, 1
	v_pk_mul_f32 v[102:103], v[210:211], v[102:103] op_sel_hi:[0,1]
	v_lshrrev_b32_e32 v87, 16, v87
	v_add3_u32 v92, v111, v92, s44
	v_pk_fma_f32 v[128:129], v[102:103], v[6:7], v[128:129]
	v_and_or_b32 v87, v92, s33, v87
	global_store_dwordx2 v[78:79], v[86:87], off offset:512 nt
	v_bfe_u32 v86, v128, 16, 1
	v_pk_mul_f32 v[104:105], v[210:211], v[104:105] op_sel_hi:[0,1]
	v_add3_u32 v86, v128, v86, s44
	v_bfe_u32 v87, v129, 16, 1
	v_pk_fma_f32 v[130:131], v[104:105], v[8:9], v[130:131]
	v_lshrrev_b32_e32 v86, 16, v86
	v_add3_u32 v87, v129, v87, s44
	v_and_or_b32 v86, v87, s33, v86
	v_bfe_u32 v87, v130, 16, 1
	v_add3_u32 v87, v130, v87, s44
	v_bfe_u32 v92, v131, 16, 1
	v_lshrrev_b32_e32 v87, 16, v87
	v_add3_u32 v92, v131, v92, s44
	v_and_or_b32 v87, v92, s33, v87
	global_store_dwordx2 v[78:79], v[86:87], off offset:1024 nt
	v_bfe_u32 v86, v124, 16, 1
	v_pk_mul_f32 v[96:97], v[210:211], v[96:97] op_sel_hi:[0,1]
	v_add3_u32 v86, v124, v86, s44
	v_bfe_u32 v87, v125, 16, 1
	v_pk_fma_f32 v[96:97], v[96:97], v[24:25], v[126:127]
	v_lshrrev_b32_e32 v86, 16, v86
	v_add3_u32 v87, v125, v87, s44
	v_and_or_b32 v86, v87, s33, v86
	v_bfe_u32 v87, v96, 16, 1
	v_add3_u32 v87, v96, v87, s44
	v_bfe_u32 v92, v97, 16, 1
	v_lshrrev_b32_e32 v87, 16, v87
	v_add3_u32 v92, v97, v92, s44
	v_and_or_b32 v87, v92, s33, v87
	global_store_dwordx2 v[78:79], v[86:87], off offset:1536 nt
	v_bfe_u32 v86, v90, 16, 1
	v_add3_u32 v86, v90, v86, s44
	v_bfe_u32 v87, v91, 16, 1
	v_pk_fma_f32 v[88:89], v[88:89], v[28:29], v[122:123]
	v_lshrrev_b32_e32 v86, 16, v86
	v_add3_u32 v87, v91, v87, s44
	v_and_or_b32 v86, v87, s33, v86
	v_bfe_u32 v87, v88, 16, 1
	v_add3_u32 v87, v88, v87, s44
	v_bfe_u32 v92, v89, 16, 1
	v_lshrrev_b32_e32 v87, 16, v87
	v_add3_u32 v92, v89, v92, s44
	v_pk_fma_f32 v[108:109], v[94:95], v[30:31], v[108:109]
	v_and_or_b32 v87, v92, s33, v87
	global_store_dwordx2 v[78:79], v[86:87], off offset:2048 nt
	v_bfe_u32 v86, v108, 16, 1
	v_add3_u32 v86, v108, v86, s44
	v_bfe_u32 v87, v109, 16, 1
	v_lshrrev_b32_e32 v86, 16, v86
	v_add3_u32 v87, v109, v87, s44
	v_and_or_b32 v86, v87, s33, v86
	v_bfe_u32 v87, v84, 16, 1
	v_add3_u32 v87, v84, v87, s44
	v_bfe_u32 v92, v85, 16, 1
	v_lshrrev_b32_e32 v87, 16, v87
	v_add3_u32 v92, v85, v92, s44
	v_and_or_b32 v87, v92, s33, v87
	global_store_dwordx2 v[78:79], v[86:87], off offset:2560 nt
	v_bfe_u32 v86, v82, 16, 1
	v_add3_u32 v86, v82, v86, s44
	v_bfe_u32 v87, v83, 16, 1
	v_pk_fma_f32 v[80:81], v[80:81], v[36:37], v[106:107]
	v_lshrrev_b32_e32 v86, 16, v86
	v_add3_u32 v87, v83, v87, s44
	v_and_or_b32 v86, v87, s33, v86
	v_bfe_u32 v87, v80, 16, 1
	v_add3_u32 v87, v80, v87, s44
	v_bfe_u32 v92, v81, 16, 1
	v_lshrrev_b32_e32 v87, 16, v87
	v_add3_u32 v92, v81, v92, s44
	v_and_or_b32 v87, v92, s33, v87
	v_mul_f32_e32 v92, v121, v121
	v_mul_f32_e32 v93, v119, v119
	v_fmac_f32_e32 v92, v120, v120
	v_fmac_f32_e32 v93, v118, v118
	v_add_f32_e32 v92, v92, v93
	v_mul_f32_e32 v93, v113, v113
	v_mul_f32_e32 v94, v111, v111
	v_fmac_f32_e32 v93, v112, v112
	v_fmac_f32_e32 v94, v110, v110
	v_add_f32_e32 v93, v93, v94
	v_add_f32_e32 v92, v92, v93
	v_mul_f32_e32 v93, v129, v129
	v_mul_f32_e32 v94, v131, v131
	v_fmac_f32_e32 v93, v128, v128
	v_fmac_f32_e32 v94, v130, v130
	v_add_f32_e32 v93, v93, v94
	v_add_f32_e32 v92, v92, v93
	v_mul_f32_e32 v93, v125, v125
	v_mul_f32_e32 v94, v97, v97
	v_fmac_f32_e32 v93, v124, v124
	v_fmac_f32_e32 v94, v96, v96
	v_add_f32_e32 v93, v93, v94
	v_add_f32_e32 v92, v92, v93
	v_mul_f32_e32 v93, v91, v91
	v_mul_f32_e32 v94, v89, v89
	v_fmac_f32_e32 v93, v90, v90
	v_fmac_f32_e32 v94, v88, v88
	v_add_f32_e32 v93, v93, v94
	v_add_f32_e32 v92, v92, v93
	v_mul_f32_e32 v93, v109, v109
	v_mul_f32_e32 v94, v85, v85
	v_fmac_f32_e32 v93, v108, v108
	v_fmac_f32_e32 v94, v84, v84
	v_add_f32_e32 v93, v93, v94
	v_add_f32_e32 v92, v92, v93
	v_mul_f32_e32 v93, v83, v83
	v_mul_f32_e32 v94, v81, v81
	v_fmac_f32_e32 v93, v82, v82
	v_fmac_f32_e32 v94, v80, v80
	v_pk_fma_f32 v[76:77], v[76:77], v[40:41], v[98:99]
	v_add_f32_e32 v93, v93, v94
	v_add_f32_e32 v92, v92, v93
	v_mul_f32_e32 v93, v115, v115
	v_mul_f32_e32 v94, v77, v77
	v_fmac_f32_e32 v93, v114, v114
	v_fmac_f32_e32 v94, v76, v76
	v_add_f32_e32 v93, v93, v94
	v_add_f32_e32 v92, v92, v93
	v_mov_b32_e32 v93, 0
	global_store_dwordx2 v[78:79], v[86:87], off offset:3072 nt
	v_add_f32_dpp v92, v92, v92 quad_perm:[1,0,3,2] row_mask:0xf bank_mask:0xf bound_ctrl:1
	v_bfe_u32 v86, v114, 16, 1
	v_add3_u32 v86, v114, v86, s44
	v_add_f32_dpp v92, v92, v92 quad_perm:[2,3,0,1] row_mask:0xf bank_mask:0xf bound_ctrl:1
	v_bfe_u32 v87, v115, 16, 1
	v_lshrrev_b32_e32 v86, 16, v86
	v_add_f32_dpp v92, v92, v92 row_half_mirror row_mask:0xf bank_mask:0xf bound_ctrl:1
	v_add3_u32 v87, v115, v87, s44
	v_and_or_b32 v86, v87, s33, v86
	v_add_f32_dpp v92, v92, v92 row_mirror row_mask:0xf bank_mask:0xf bound_ctrl:1
	v_bfe_u32 v87, v76, 16, 1
	v_add3_u32 v87, v76, v87, s44
	v_mov_b32_dpp v93, v92 row_bcast:15 row_mask:0xa bank_mask:0xf
	v_add_f32_e32 v92, v92, v93
	v_mov_b32_e32 v93, 0
	v_bfe_u32 v94, v77, 16, 1
	v_lshrrev_b32_e32 v87, 16, v87
	v_mov_b32_dpp v93, v92 row_bcast:31 row_mask:0xc bank_mask:0xf
	v_add_f32_e32 v92, v92, v93
	v_add3_u32 v94, v77, v94, s44
	v_readlane_b32 s0, v92, 63
	v_and_or_b32 v87, v94, s33, v87
	global_store_dwordx2 v[78:79], v[86:87], off offset:3584 nt
	v_fma_f32 v92, s0, v142, v66
	v_mul_f32_e32 v93, 0x4f800000, v92
	v_cmp_gt_f32_e32 vcc, s45, v92
	s_nop 1
	v_cndmask_b32_e32 v92, v92, v93, vcc
	v_sqrt_f32_e32 v93, v92
	s_nop 0
	v_add_u32_e32 v95, -1, v93
	v_fma_f32 v98, -v95, v93, v92
	v_cmp_ge_f32_e64 s[0:1], 0, v98
	v_add_u32_e32 v98, 1, v93
	s_nop 0
	v_cndmask_b32_e64 v95, v93, v95, s[0:1]
	v_fma_f32 v93, -v98, v93, v92
	v_cmp_lt_f32_e64 s[0:1], 0, v93
	s_nop 1
	v_cndmask_b32_e64 v93, v95, v98, s[0:1]
	v_mul_f32_e32 v95, 0x37800000, v93
	v_cndmask_b32_e32 v93, v93, v95, vcc
	v_cmp_class_f32_e32 vcc, v92, v140
	s_nop 1
	v_cndmask_b32_e32 v92, v93, v92, vcc
	v_div_scale_f32 v93, s[0:1], v92, v92, 1.0
	v_rcp_f32_e32 v95, v93
	s_nop 0
	v_fma_f32 v78, -v93, v95, 1.0
	v_fmac_f32_e32 v95, v78, v95
	v_div_scale_f32 v78, vcc, 1.0, v92, 1.0
	v_mul_f32_e32 v79, v78, v95
	v_fma_f32 v86, -v93, v79, v78
	v_fmac_f32_e32 v79, v86, v95
	v_fma_f32 v78, -v93, v79, v78
	v_div_fmas_f32 v78, v78, v95, v79
	v_div_fixup_f32 v116, v78, v92, 1.0
	v_pk_mul_f32 v[78:79], v[116:117], v[120:121] op_sel_hi:[0,1]
	v_pk_mul_f32 v[86:87], v[116:117], v[118:119] op_sel_hi:[0,1]
	v_pk_mul_f32 v[106:107], v[78:79], v[42:43]
	v_pk_mul_f32 v[78:79], v[116:117], v[112:113] op_sel_hi:[0,1]
	v_pk_mul_f32 v[102:103], v[86:87], v[44:45]
	v_pk_mul_f32 v[86:87], v[116:117], v[110:111] op_sel_hi:[0,1]
	v_pk_mul_f32 v[104:105], v[78:79], v[10:11]
	v_pk_mul_f32 v[78:79], v[116:117], v[128:129] op_sel_hi:[0,1]
	v_pk_mul_f32 v[100:101], v[86:87], v[12:13]
	v_pk_mul_f32 v[86:87], v[116:117], v[130:131] op_sel_hi:[0,1]
	v_pk_mul_f32 v[98:99], v[78:79], v[14:15]
	v_pk_mul_f32 v[78:79], v[116:117], v[124:125] op_sel_hi:[0,1]
	v_pk_mul_f32 v[94:95], v[86:87], v[16:17]
	v_pk_mul_f32 v[86:87], v[116:117], v[96:97] op_sel_hi:[0,1]
	v_pk_mul_f32 v[96:97], v[78:79], v[46:47]
	v_pk_mul_f32 v[78:79], v[116:117], v[90:91] op_sel_hi:[0,1]
	v_pk_mul_f32 v[90:91], v[78:79], v[50:51]
	v_pk_mul_f32 v[78:79], v[116:117], v[108:109] op_sel_hi:[0,1]
	v_mul_f32_e32 v110, 0x41800000, v106
	v_mul_f32_e32 v111, 0x41800000, v107
	v_pk_mul_f32 v[92:93], v[86:87], v[48:49]
	v_pk_mul_f32 v[86:87], v[116:117], v[88:89] op_sel_hi:[0,1]
	v_pk_mul_f32 v[88:89], v[78:79], v[54:55]
	v_pk_mul_f32 v[78:79], v[116:117], v[80:81] op_sel_hi:[0,1]
	v_pk_mul_f32 v[80:81], v[116:117], v[114:115] op_sel_hi:[0,1]
	v_med3_f32 v110, v110, s47, v143
	v_med3_f32 v111, v111, s47, v143
	v_mov_b32_e32 v114, 0
	v_cvt_pk_fp8_f32 v114, v110, v111
	v_lshl_add_u64 v[108:109], s[86:87], 0, v[72:73]
	v_mul_f32_e32 v112, 0x41800000, v102
	v_mul_f32_e32 v110, 0x41800000, v103
	v_med3_f32 v111, v112, s47, v143
	v_add_co_u32_e32 v112, vcc, s48, v108
	v_med3_f32 v110, v110, s47, v143
	s_nop 0
	v_addc_co_u32_e32 v113, vcc, 0, v109, vcc
	v_mul_f32_e32 v108, 0x41800000, v104
	v_mul_f32_e32 v109, 0x41800000, v105
	v_cvt_pk_fp8_f32 v114, v111, v110 op_sel:[0,0,1]
	v_med3_f32 v108, v108, s47, v143
	v_med3_f32 v109, v109, s47, v143
	v_mov_b32_e32 v111, 0
	v_cvt_pk_fp8_f32 v111, v108, v109
	v_mul_f32_e32 v110, 0x41800000, v100
	v_mul_f32_e32 v108, 0x41800000, v101
	v_med3_f32 v109, v110, s47, v143
	v_med3_f32 v108, v108, s47, v143
	v_cvt_pk_fp8_f32 v111, v109, v108 op_sel:[0,0,1]
	v_mul_f32_e32 v108, 0x41800000, v98
	v_mul_f32_e32 v109, 0x41800000, v99
	global_store_dword v[112:113], v114, off
	v_med3_f32 v108, v108, s47, v143
	v_med3_f32 v109, v109, s47, v143
	v_mov_b32_e32 v114, 0
	v_cvt_pk_fp8_f32 v114, v108, v109
	v_mul_f32_e32 v110, 0x41800000, v94
	v_mul_f32_e32 v108, 0x41800000, v95
	v_med3_f32 v109, v110, s47, v143
	v_med3_f32 v108, v108, s47, v143
	v_cvt_pk_fp8_f32 v114, v109, v108 op_sel:[0,0,1]
	v_mul_f32_e32 v108, 0x41800000, v96
	v_mul_f32_e32 v109, 0x41800000, v97
	v_med3_f32 v108, v108, s47, v143
	v_med3_f32 v109, v109, s47, v143
	v_mov_b32_e32 v115, 0
	v_cvt_pk_fp8_f32 v115, v108, v109
	v_mul_f32_e32 v110, 0x41800000, v92
	v_mul_f32_e32 v108, 0x41800000, v93
	v_med3_f32 v109, v110, s47, v143
	v_med3_f32 v108, v108, s47, v143
	v_cvt_pk_fp8_f32 v115, v109, v108 op_sel:[0,0,1]
	v_mul_f32_e32 v108, 0x41800000, v90
	v_mul_f32_e32 v109, 0x41800000, v91
	v_pk_mul_f32 v[84:85], v[116:117], v[84:85] op_sel_hi:[0,1]
	v_pk_mul_f32 v[82:83], v[116:117], v[82:83] op_sel_hi:[0,1]
	v_pk_mul_f32 v[76:77], v[116:117], v[76:77] op_sel_hi:[0,1]
	v_med3_f32 v108, v108, s47, v143
	v_med3_f32 v109, v109, s47, v143
	v_mov_b32_e32 v116, 0
	v_cvt_pk_fp8_f32 v116, v108, v109
	v_pk_mul_f32 v[86:87], v[86:87], v[52:53]
	v_pk_mul_f32 v[84:85], v[84:85], v[56:57]
	v_mul_f32_e32 v110, 0x41800000, v86
	v_mul_f32_e32 v108, 0x41800000, v87
	v_med3_f32 v109, v110, s47, v143
	v_med3_f32 v108, v108, s47, v143
	v_cvt_pk_fp8_f32 v116, v109, v108 op_sel:[0,0,1]
	v_mul_f32_e32 v108, 0x41800000, v88
	v_mul_f32_e32 v109, 0x41800000, v89
	global_store_dword v[112:113], v111, off offset:256
	global_store_dword v[112:113], v114, off offset:512
	global_store_dword v[112:113], v115, off offset:768
	global_store_dword v[112:113], v116, off offset:1024
	v_med3_f32 v108, v108, s47, v143
	v_med3_f32 v109, v109, s47, v143
	v_mov_b32_e32 v114, 0
	v_cvt_pk_fp8_f32 v114, v108, v109
	v_mul_f32_e32 v110, 0x41800000, v84
	v_mul_f32_e32 v108, 0x41800000, v85
	v_pk_mul_f32 v[82:83], v[82:83], v[58:59]
	v_med3_f32 v109, v110, s47, v143
	v_med3_f32 v108, v108, s47, v143
	v_cvt_pk_fp8_f32 v114, v109, v108 op_sel:[0,0,1]
	v_mul_f32_e32 v108, 0x41800000, v82
	v_mul_f32_e32 v109, 0x41800000, v83
	v_med3_f32 v108, v108, s47, v143
	v_med3_f32 v109, v109, s47, v143
	v_mov_b32_e32 v115, 0
	v_cvt_pk_fp8_f32 v115, v108, v109
	v_pk_mul_f32 v[78:79], v[78:79], v[60:61]
	v_pk_mul_f32 v[80:81], v[80:81], v[62:63]
	v_mul_f32_e32 v110, 0x41800000, v78
	v_mul_f32_e32 v108, 0x41800000, v79
	v_med3_f32 v109, v110, s47, v143
	v_med3_f32 v108, v108, s47, v143
	v_cvt_pk_fp8_f32 v115, v109, v108 op_sel:[0,0,1]
	v_mul_f32_e32 v108, 0x41800000, v80
	v_mul_f32_e32 v109, 0x41800000, v81
	v_med3_f32 v108, v108, s47, v143
	v_med3_f32 v109, v109, s47, v143
	v_mov_b32_e32 v116, 0
	v_cvt_pk_fp8_f32 v116, v108, v109
	v_pk_mul_f32 v[76:77], v[76:77], v[64:65]
	s_nop 0
	v_mul_f32_e32 v110, 0x41800000, v76
	v_mul_f32_e32 v108, 0x41800000, v77
	v_med3_f32 v109, v110, s47, v143
	v_med3_f32 v108, v108, s47, v143
	v_cvt_pk_fp8_f32 v116, v109, v108 op_sel:[0,0,1]
	ds_read_b128 v[108:111], v1
	global_store_dword v[112:113], v114, off offset:1280
	global_store_dword v[112:113], v115, off offset:1536
	global_store_dword v[112:113], v116, off offset:1792
	ds_read_b128 v[112:115], v1 offset:1024
	s_waitcnt lgkmcnt(1)
	v_mul_f32_e32 v109, v109, v107
	v_fmac_f32_e32 v109, v108, v106
	v_mul_f32_e32 v108, v111, v103
	v_fmac_f32_e32 v108, v110, v102
	v_add_f32_e32 v108, v109, v108
	v_add_f32_e32 v116, 0, v108
	ds_read_b128 v[108:111], v1 offset:2048
	s_waitcnt lgkmcnt(1)
	v_mul_f32_e32 v113, v113, v105
	v_fmac_f32_e32 v113, v112, v104
	v_mul_f32_e32 v112, v115, v101
	v_fmac_f32_e32 v112, v114, v100
	v_add_f32_e32 v112, v113, v112
	v_add_f32_e32 v116, v116, v112
	ds_read_b128 v[112:115], v1 offset:3072
	s_waitcnt lgkmcnt(1)
	v_mul_f32_e32 v109, v109, v99
	v_fmac_f32_e32 v109, v108, v98
	v_mul_f32_e32 v108, v111, v95
	v_fmac_f32_e32 v108, v110, v94
	v_add_f32_e32 v108, v109, v108
	v_add_f32_e32 v116, v116, v108
	ds_read_b128 v[108:111], v1 offset:4096
	s_waitcnt lgkmcnt(1)
	v_mul_f32_e32 v113, v113, v97
	v_fmac_f32_e32 v113, v112, v96
	v_mul_f32_e32 v112, v115, v93
	v_fmac_f32_e32 v112, v114, v92
	v_add_f32_e32 v112, v113, v112
	v_add_f32_e32 v116, v116, v112
	ds_read_b128 v[112:115], v1 offset:5120
	s_waitcnt lgkmcnt(1)
	v_mul_f32_e32 v109, v109, v91
	v_fmac_f32_e32 v109, v108, v90
	v_mul_f32_e32 v108, v111, v87
	v_fmac_f32_e32 v108, v110, v86
	v_add_f32_e32 v108, v109, v108
	v_add_f32_e32 v116, v116, v108
	ds_read_b128 v[108:111], v1 offset:6144
	s_waitcnt lgkmcnt(1)
	v_mul_f32_e32 v113, v113, v89
	v_fmac_f32_e32 v113, v112, v88
	v_mul_f32_e32 v112, v115, v85
	v_fmac_f32_e32 v112, v114, v84
	v_add_f32_e32 v112, v113, v112
	v_add_f32_e32 v116, v116, v112
	ds_read_b128 v[112:115], v1 offset:7168
	s_waitcnt lgkmcnt(1)
	v_mul_f32_e32 v109, v109, v83
	v_fmac_f32_e32 v109, v108, v82
	v_mul_f32_e32 v108, v111, v79
	v_fmac_f32_e32 v108, v110, v78
	v_add_f32_e32 v108, v109, v108
	s_waitcnt lgkmcnt(0)
	v_mul_f32_e32 v109, v113, v81
	v_mul_f32_e32 v110, v115, v77
	v_fmac_f32_e32 v109, v112, v80
	v_fmac_f32_e32 v110, v114, v76
	v_add_f32_e32 v108, v116, v108
	v_add_f32_e32 v109, v109, v110
	v_add_f32_e32 v108, v108, v109
	v_mov_b32_e32 v109, 0
	v_mov_b32_e32 v113, 0
	v_add_f32_dpp v108, v108, v108 quad_perm:[1,0,3,2] row_mask:0xf bank_mask:0xf bound_ctrl:1
	s_nop 1
	v_add_f32_dpp v108, v108, v108 quad_perm:[2,3,0,1] row_mask:0xf bank_mask:0xf bound_ctrl:1
	s_nop 1
	v_add_f32_dpp v108, v108, v108 row_half_mirror row_mask:0xf bank_mask:0xf bound_ctrl:1
	s_nop 1
	v_add_f32_dpp v108, v108, v108 row_mirror row_mask:0xf bank_mask:0xf bound_ctrl:1
	s_nop 1
	v_mov_b32_dpp v109, v108 row_bcast:15 row_mask:0xa bank_mask:0xf
	v_add_f32_e32 v112, v108, v109
	ds_read_b128 v[108:111], v1 offset:8192
	s_nop 0
	v_mov_b32_dpp v113, v112 row_bcast:31 row_mask:0xc bank_mask:0xf
	v_add_f32_e32 v112, v112, v113
	s_nop 0
	v_readlane_b32 s16, v112, 63
	ds_read_b128 v[112:115], v1 offset:9216
	s_waitcnt lgkmcnt(1)
	v_mul_f32_e32 v109, v109, v107
	v_fmac_f32_e32 v109, v108, v106
	v_mul_f32_e32 v108, v111, v103
	v_fmac_f32_e32 v108, v110, v102
	v_add_f32_e32 v108, v109, v108
	s_waitcnt lgkmcnt(0)
	v_mul_f32_e32 v113, v113, v105
	v_add_f32_e32 v116, 0, v108
	v_fmac_f32_e32 v113, v112, v104
	v_mul_f32_e32 v112, v115, v101
	ds_read_b128 v[108:111], v1 offset:10240
	v_fmac_f32_e32 v112, v114, v100
	v_add_f32_e32 v112, v113, v112
	v_add_f32_e32 v116, v116, v112
	ds_read_b128 v[112:115], v1 offset:11264
	s_waitcnt lgkmcnt(1)
	v_mul_f32_e32 v109, v109, v99
	v_fmac_f32_e32 v109, v108, v98
	v_mul_f32_e32 v108, v111, v95
	v_fmac_f32_e32 v108, v110, v94
	v_add_f32_e32 v108, v109, v108
	s_waitcnt lgkmcnt(0)
	v_mul_f32_e32 v113, v113, v97
	v_add_f32_e32 v116, v116, v108
	v_fmac_f32_e32 v113, v112, v96
	v_mul_f32_e32 v112, v115, v93
	ds_read_b128 v[108:111], v1 offset:12288
	v_fmac_f32_e32 v112, v114, v92
	v_add_f32_e32 v112, v113, v112
	v_add_f32_e32 v116, v116, v112
	ds_read_b128 v[112:115], v1 offset:13312
	s_waitcnt lgkmcnt(1)
	v_mul_f32_e32 v109, v109, v91
	v_fmac_f32_e32 v109, v108, v90
	v_mul_f32_e32 v108, v111, v87
	v_fmac_f32_e32 v108, v110, v86
	v_add_f32_e32 v108, v109, v108
	s_waitcnt lgkmcnt(0)
	v_mul_f32_e32 v113, v113, v89
	v_add_f32_e32 v116, v116, v108
	v_fmac_f32_e32 v113, v112, v88
	v_mul_f32_e32 v112, v115, v85
	ds_read_b128 v[108:111], v1 offset:14336
	v_fmac_f32_e32 v112, v114, v84
	v_add_f32_e32 v112, v113, v112
	v_add_f32_e32 v116, v116, v112
	ds_read_b128 v[112:115], v1 offset:15360
	s_waitcnt lgkmcnt(1)
	v_mul_f32_e32 v109, v109, v83
	v_fmac_f32_e32 v109, v108, v82
	v_mul_f32_e32 v108, v111, v79
	v_fmac_f32_e32 v108, v110, v78
	v_add_f32_e32 v108, v109, v108
	s_waitcnt lgkmcnt(0)
	v_mul_f32_e32 v109, v113, v81
	v_mul_f32_e32 v110, v115, v77
	v_fmac_f32_e32 v109, v112, v80
	v_fmac_f32_e32 v110, v114, v76
	v_add_f32_e32 v108, v116, v108
	v_add_f32_e32 v109, v109, v110
	v_add_f32_e32 v108, v108, v109
	v_mov_b32_e32 v109, 0
	v_mov_b32_e32 v113, 0
	v_add_f32_dpp v108, v108, v108 quad_perm:[1,0,3,2] row_mask:0xf bank_mask:0xf bound_ctrl:1
	s_nop 1
	v_add_f32_dpp v108, v108, v108 quad_perm:[2,3,0,1] row_mask:0xf bank_mask:0xf bound_ctrl:1
	s_nop 1
	v_add_f32_dpp v108, v108, v108 row_half_mirror row_mask:0xf bank_mask:0xf bound_ctrl:1
	s_nop 1
	v_add_f32_dpp v108, v108, v108 row_mirror row_mask:0xf bank_mask:0xf bound_ctrl:1
	s_nop 1
	v_mov_b32_dpp v109, v108 row_bcast:15 row_mask:0xa bank_mask:0xf
	v_add_f32_e32 v112, v108, v109
	ds_read_b128 v[108:111], v1 offset:16384
	s_nop 0
	v_mov_b32_dpp v113, v112 row_bcast:31 row_mask:0xc bank_mask:0xf
	v_add_f32_e32 v112, v112, v113
	s_nop 0
	v_readlane_b32 s17, v112, 63
	ds_read_b128 v[112:115], v1 offset:17408
	s_waitcnt lgkmcnt(1)
	v_mul_f32_e32 v109, v109, v107
	v_fmac_f32_e32 v109, v108, v106
	v_mul_f32_e32 v108, v111, v103
	v_fmac_f32_e32 v108, v110, v102
	v_add_f32_e32 v108, v109, v108
	s_waitcnt lgkmcnt(0)
	v_mul_f32_e32 v113, v113, v105
	v_add_f32_e32 v116, 0, v108
	v_fmac_f32_e32 v113, v112, v104
	v_mul_f32_e32 v112, v115, v101
	ds_read_b128 v[108:111], v1 offset:18432
	v_fmac_f32_e32 v112, v114, v100
	v_add_f32_e32 v112, v113, v112
	v_add_f32_e32 v116, v116, v112
	ds_read_b128 v[112:115], v1 offset:19456
	s_waitcnt lgkmcnt(1)
	v_mul_f32_e32 v109, v109, v99
	v_fmac_f32_e32 v109, v108, v98
	v_mul_f32_e32 v108, v111, v95
	v_fmac_f32_e32 v108, v110, v94
	v_add_f32_e32 v108, v109, v108
	s_waitcnt lgkmcnt(0)
	v_mul_f32_e32 v113, v113, v97
	v_add_f32_e32 v116, v116, v108
	v_fmac_f32_e32 v113, v112, v96
	v_mul_f32_e32 v112, v115, v93
	ds_read_b128 v[108:111], v1 offset:20480
	v_fmac_f32_e32 v112, v114, v92
	v_add_f32_e32 v112, v113, v112
	v_add_f32_e32 v116, v116, v112
	ds_read_b128 v[112:115], v1 offset:21504
	s_waitcnt lgkmcnt(1)
	v_mul_f32_e32 v109, v109, v91
	v_fmac_f32_e32 v109, v108, v90
	v_mul_f32_e32 v108, v111, v87
	v_fmac_f32_e32 v108, v110, v86
	v_add_f32_e32 v108, v109, v108
	s_waitcnt lgkmcnt(0)
	v_mul_f32_e32 v113, v113, v89
	v_add_f32_e32 v116, v116, v108
	v_fmac_f32_e32 v113, v112, v88
	v_mul_f32_e32 v112, v115, v85
	ds_read_b128 v[108:111], v1 offset:22528
	v_fmac_f32_e32 v112, v114, v84
	v_add_f32_e32 v112, v113, v112
	v_add_f32_e32 v116, v116, v112
	ds_read_b128 v[112:115], v1 offset:23552
	s_waitcnt lgkmcnt(1)
	v_mul_f32_e32 v109, v109, v83
	v_fmac_f32_e32 v109, v108, v82
	v_mul_f32_e32 v108, v111, v79
	v_fmac_f32_e32 v108, v110, v78
	v_add_f32_e32 v108, v109, v108
	s_waitcnt lgkmcnt(0)
	v_mul_f32_e32 v109, v113, v81
	v_mul_f32_e32 v110, v115, v77
	v_fmac_f32_e32 v109, v112, v80
	v_fmac_f32_e32 v110, v114, v76
	v_add_f32_e32 v108, v116, v108
	v_add_f32_e32 v109, v109, v110
	v_add_f32_e32 v108, v108, v109
	v_mov_b32_e32 v109, 0
	v_mov_b32_e32 v113, 0
	v_add_f32_dpp v108, v108, v108 quad_perm:[1,0,3,2] row_mask:0xf bank_mask:0xf bound_ctrl:1
	s_nop 1
	v_add_f32_dpp v108, v108, v108 quad_perm:[2,3,0,1] row_mask:0xf bank_mask:0xf bound_ctrl:1
	s_nop 1
	v_add_f32_dpp v108, v108, v108 row_half_mirror row_mask:0xf bank_mask:0xf bound_ctrl:1
	s_nop 1
	v_add_f32_dpp v108, v108, v108 row_mirror row_mask:0xf bank_mask:0xf bound_ctrl:1
	s_nop 1
	v_mov_b32_dpp v109, v108 row_bcast:15 row_mask:0xa bank_mask:0xf
	v_add_f32_e32 v112, v108, v109
	ds_read_b128 v[108:111], v1 offset:24576
	s_nop 0
	v_mov_b32_dpp v113, v112 row_bcast:31 row_mask:0xc bank_mask:0xf
	v_add_f32_e32 v112, v112, v113
	s_nop 0
	v_readlane_b32 s35, v112, 63
	ds_read_b128 v[112:115], v1 offset:25600
	s_waitcnt lgkmcnt(1)
	v_mul_f32_e32 v109, v109, v107
	v_fmac_f32_e32 v109, v108, v106
	v_mul_f32_e32 v108, v111, v103
	v_fmac_f32_e32 v108, v110, v102
	v_add_f32_e32 v108, v109, v108
	s_waitcnt lgkmcnt(0)
	v_mul_f32_e32 v113, v113, v105
	v_add_f32_e32 v116, 0, v108
	v_fmac_f32_e32 v113, v112, v104
	v_mul_f32_e32 v112, v115, v101
	ds_read_b128 v[108:111], v1 offset:26624
	v_fmac_f32_e32 v112, v114, v100
	v_add_f32_e32 v112, v113, v112
	v_add_f32_e32 v116, v116, v112
	ds_read_b128 v[112:115], v1 offset:27648
	s_waitcnt lgkmcnt(1)
	v_mul_f32_e32 v109, v109, v99
	v_fmac_f32_e32 v109, v108, v98
	v_mul_f32_e32 v108, v111, v95
	v_fmac_f32_e32 v108, v110, v94
	v_add_f32_e32 v108, v109, v108
	s_waitcnt lgkmcnt(0)
	v_mul_f32_e32 v113, v113, v97
	v_add_f32_e32 v116, v116, v108
	v_fmac_f32_e32 v113, v112, v96
	v_mul_f32_e32 v112, v115, v93
	ds_read_b128 v[108:111], v1 offset:28672
	v_fmac_f32_e32 v112, v114, v92
	v_add_f32_e32 v112, v113, v112
	v_add_f32_e32 v116, v116, v112
	ds_read_b128 v[112:115], v1 offset:29696
	s_waitcnt lgkmcnt(1)
	v_mul_f32_e32 v109, v109, v91
	v_fmac_f32_e32 v109, v108, v90
	v_mul_f32_e32 v108, v111, v87
	v_fmac_f32_e32 v108, v110, v86
	v_add_f32_e32 v108, v109, v108
	s_waitcnt lgkmcnt(0)
	v_mul_f32_e32 v113, v113, v89
	v_add_f32_e32 v116, v116, v108
	v_fmac_f32_e32 v113, v112, v88
	v_mul_f32_e32 v112, v115, v85
	ds_read_b128 v[108:111], v1 offset:30720
	v_fmac_f32_e32 v112, v114, v84
	v_add_f32_e32 v112, v113, v112
	v_add_f32_e32 v116, v116, v112
	ds_read_b128 v[112:115], v1 offset:31744
	s_waitcnt lgkmcnt(1)
	v_mul_f32_e32 v109, v109, v83
	v_fmac_f32_e32 v109, v108, v82
	v_mul_f32_e32 v108, v111, v79
	v_fmac_f32_e32 v108, v110, v78
	v_add_f32_e32 v108, v109, v108
	s_waitcnt lgkmcnt(0)
	v_mul_f32_e32 v109, v113, v81
	v_mul_f32_e32 v110, v115, v77
	v_fmac_f32_e32 v109, v112, v80
	v_fmac_f32_e32 v110, v114, v76
	v_add_f32_e32 v108, v116, v108
	v_add_f32_e32 v109, v109, v110
	v_add_f32_e32 v108, v108, v109
	v_mov_b32_e32 v109, 0
	v_mov_b32_e32 v113, 0
	v_add_f32_dpp v108, v108, v108 quad_perm:[1,0,3,2] row_mask:0xf bank_mask:0xf bound_ctrl:1
	s_nop 1
	v_add_f32_dpp v108, v108, v108 quad_perm:[2,3,0,1] row_mask:0xf bank_mask:0xf bound_ctrl:1
	s_nop 1
	v_add_f32_dpp v108, v108, v108 row_half_mirror row_mask:0xf bank_mask:0xf bound_ctrl:1
	s_nop 1
	v_add_f32_dpp v108, v108, v108 row_mirror row_mask:0xf bank_mask:0xf bound_ctrl:1
	s_nop 1
	v_mov_b32_dpp v109, v108 row_bcast:15 row_mask:0xa bank_mask:0xf
	v_add_f32_e32 v112, v108, v109
	ds_read_b128 v[108:111], v1 offset:32768
	s_nop 0
	v_mov_b32_dpp v113, v112 row_bcast:31 row_mask:0xc bank_mask:0xf
	v_add_f32_e32 v112, v112, v113
	s_nop 0
	v_readlane_b32 s52, v112, 63
	ds_read_b128 v[112:115], v1 offset:33792
	s_waitcnt lgkmcnt(1)
	v_mul_f32_e32 v109, v109, v107
	v_fmac_f32_e32 v109, v108, v106
	v_mul_f32_e32 v108, v111, v103
	v_fmac_f32_e32 v108, v110, v102
	v_add_f32_e32 v108, v109, v108
	s_waitcnt lgkmcnt(0)
	v_mul_f32_e32 v113, v113, v105
	v_add_f32_e32 v116, 0, v108
	v_fmac_f32_e32 v113, v112, v104
	v_mul_f32_e32 v112, v115, v101
	ds_read_b128 v[108:111], v1 offset:34816
	v_fmac_f32_e32 v112, v114, v100
	v_add_f32_e32 v112, v113, v112
	v_add_f32_e32 v116, v116, v112
	ds_read_b128 v[112:115], v1 offset:35840
	s_waitcnt lgkmcnt(1)
	v_mul_f32_e32 v109, v109, v99
	v_fmac_f32_e32 v109, v108, v98
	v_mul_f32_e32 v108, v111, v95
	v_fmac_f32_e32 v108, v110, v94
	v_add_f32_e32 v108, v109, v108
	s_waitcnt lgkmcnt(0)
	v_mul_f32_e32 v113, v113, v97
	v_add_f32_e32 v116, v116, v108
	v_fmac_f32_e32 v113, v112, v96
	v_mul_f32_e32 v112, v115, v93
	ds_read_b128 v[108:111], v1 offset:36864
	v_fmac_f32_e32 v112, v114, v92
	v_add_f32_e32 v112, v113, v112
	v_add_f32_e32 v116, v116, v112
	ds_read_b128 v[112:115], v1 offset:37888
	s_waitcnt lgkmcnt(1)
	v_mul_f32_e32 v109, v109, v91
	v_fmac_f32_e32 v109, v108, v90
	v_mul_f32_e32 v108, v111, v87
	v_fmac_f32_e32 v108, v110, v86
	v_add_f32_e32 v108, v109, v108
	s_waitcnt lgkmcnt(0)
	v_mul_f32_e32 v113, v113, v89
	v_add_f32_e32 v116, v116, v108
	v_fmac_f32_e32 v113, v112, v88
	v_mul_f32_e32 v112, v115, v85
	ds_read_b128 v[108:111], v1 offset:38912
	v_fmac_f32_e32 v112, v114, v84
	v_add_f32_e32 v112, v113, v112
	v_add_f32_e32 v116, v116, v112
	ds_read_b128 v[112:115], v1 offset:39936
	s_waitcnt lgkmcnt(1)
	v_mul_f32_e32 v109, v109, v83
	v_fmac_f32_e32 v109, v108, v82
	v_mul_f32_e32 v108, v111, v79
	v_fmac_f32_e32 v108, v110, v78
	v_add_f32_e32 v108, v109, v108
	s_waitcnt lgkmcnt(0)
	v_mul_f32_e32 v109, v113, v81
	v_mul_f32_e32 v110, v115, v77
	v_fmac_f32_e32 v109, v112, v80
	v_fmac_f32_e32 v110, v114, v76
	v_add_f32_e32 v108, v116, v108
	v_add_f32_e32 v109, v109, v110
	v_add_f32_e32 v108, v108, v109
	v_mov_b32_e32 v109, 0
	v_mov_b32_e32 v113, 0
	v_add_f32_dpp v108, v108, v108 quad_perm:[1,0,3,2] row_mask:0xf bank_mask:0xf bound_ctrl:1
	s_nop 1
	v_add_f32_dpp v108, v108, v108 quad_perm:[2,3,0,1] row_mask:0xf bank_mask:0xf bound_ctrl:1
	s_nop 1
	v_add_f32_dpp v108, v108, v108 row_half_mirror row_mask:0xf bank_mask:0xf bound_ctrl:1
	s_nop 1
	v_add_f32_dpp v108, v108, v108 row_mirror row_mask:0xf bank_mask:0xf bound_ctrl:1
	s_nop 1
	v_mov_b32_dpp v109, v108 row_bcast:15 row_mask:0xa bank_mask:0xf
	v_add_f32_e32 v112, v108, v109
	ds_read_b128 v[108:111], v1 offset:40960
	s_nop 0
	v_mov_b32_dpp v113, v112 row_bcast:31 row_mask:0xc bank_mask:0xf
	v_add_f32_e32 v112, v112, v113
	s_nop 0
	v_readlane_b32 s53, v112, 63
	ds_read_b128 v[112:115], v1 offset:41984
	s_waitcnt lgkmcnt(1)
	v_mul_f32_e32 v109, v109, v107
	v_fmac_f32_e32 v109, v108, v106
	v_mul_f32_e32 v108, v111, v103
	v_fmac_f32_e32 v108, v110, v102
	v_add_f32_e32 v108, v109, v108
	s_waitcnt lgkmcnt(0)
	v_mul_f32_e32 v113, v113, v105
	v_add_f32_e32 v116, 0, v108
	v_fmac_f32_e32 v113, v112, v104
	v_mul_f32_e32 v112, v115, v101
	ds_read_b128 v[108:111], v1 offset:43008
	v_fmac_f32_e32 v112, v114, v100
	v_add_f32_e32 v112, v113, v112
	v_add_f32_e32 v116, v116, v112
	ds_read_b128 v[112:115], v1 offset:44032
	s_waitcnt lgkmcnt(1)
	v_mul_f32_e32 v109, v109, v99
	v_fmac_f32_e32 v109, v108, v98
	v_mul_f32_e32 v108, v111, v95
	v_fmac_f32_e32 v108, v110, v94
	v_add_f32_e32 v108, v109, v108
	s_waitcnt lgkmcnt(0)
	v_mul_f32_e32 v113, v113, v97
	v_add_f32_e32 v116, v116, v108
	v_fmac_f32_e32 v113, v112, v96
	v_mul_f32_e32 v112, v115, v93
	ds_read_b128 v[108:111], v1 offset:45056
	v_fmac_f32_e32 v112, v114, v92
	v_add_f32_e32 v112, v113, v112
	v_add_f32_e32 v116, v116, v112
	ds_read_b128 v[112:115], v1 offset:46080
	s_waitcnt lgkmcnt(1)
	v_mul_f32_e32 v109, v109, v91
	v_fmac_f32_e32 v109, v108, v90
	v_mul_f32_e32 v108, v111, v87
	v_fmac_f32_e32 v108, v110, v86
	v_add_f32_e32 v108, v109, v108
	s_waitcnt lgkmcnt(0)
	v_mul_f32_e32 v113, v113, v89
	v_add_f32_e32 v116, v116, v108
	v_fmac_f32_e32 v113, v112, v88
	v_mul_f32_e32 v112, v115, v85
	ds_read_b128 v[108:111], v1 offset:47104
	v_fmac_f32_e32 v112, v114, v84
	v_add_f32_e32 v112, v113, v112
	v_add_f32_e32 v116, v116, v112
	ds_read_b128 v[112:115], v1 offset:48128
	s_waitcnt lgkmcnt(1)
	v_mul_f32_e32 v109, v109, v83
	v_fmac_f32_e32 v109, v108, v82
	v_mul_f32_e32 v108, v111, v79
	v_fmac_f32_e32 v108, v110, v78
	v_add_f32_e32 v108, v109, v108
	s_waitcnt lgkmcnt(0)
	v_mul_f32_e32 v109, v113, v81
	v_mul_f32_e32 v110, v115, v77
	v_fmac_f32_e32 v109, v112, v80
	v_fmac_f32_e32 v110, v114, v76
	v_add_f32_e32 v108, v116, v108
	v_add_f32_e32 v109, v109, v110
	v_add_f32_e32 v108, v108, v109
	v_mov_b32_e32 v109, 0
	v_mov_b32_e32 v113, 0
	v_add_f32_dpp v108, v108, v108 quad_perm:[1,0,3,2] row_mask:0xf bank_mask:0xf bound_ctrl:1
	s_nop 1
	v_add_f32_dpp v108, v108, v108 quad_perm:[2,3,0,1] row_mask:0xf bank_mask:0xf bound_ctrl:1
	s_nop 1
	v_add_f32_dpp v108, v108, v108 row_half_mirror row_mask:0xf bank_mask:0xf bound_ctrl:1
	s_nop 1
	v_add_f32_dpp v108, v108, v108 row_mirror row_mask:0xf bank_mask:0xf bound_ctrl:1
	s_nop 1
	v_mov_b32_dpp v109, v108 row_bcast:15 row_mask:0xa bank_mask:0xf
	v_add_f32_e32 v112, v108, v109
	ds_read_b128 v[108:111], v1 offset:49152
	s_nop 0
	v_mov_b32_dpp v113, v112 row_bcast:31 row_mask:0xc bank_mask:0xf
	v_add_f32_e32 v112, v112, v113
	s_nop 0
	v_readlane_b32 s54, v112, 63
	ds_read_b128 v[112:115], v1 offset:50176
	s_waitcnt lgkmcnt(1)
	v_mul_f32_e32 v109, v109, v107
	v_fmac_f32_e32 v109, v108, v106
	v_mul_f32_e32 v108, v111, v103
	v_fmac_f32_e32 v108, v110, v102
	v_add_f32_e32 v108, v109, v108
	s_waitcnt lgkmcnt(0)
	v_mul_f32_e32 v113, v113, v105
	v_add_f32_e32 v116, 0, v108
	v_fmac_f32_e32 v113, v112, v104
	v_mul_f32_e32 v112, v115, v101
	ds_read_b128 v[108:111], v1 offset:51200
	v_fmac_f32_e32 v112, v114, v100
	v_add_f32_e32 v112, v113, v112
	v_add_f32_e32 v116, v116, v112
	ds_read_b128 v[112:115], v1 offset:52224
	s_waitcnt lgkmcnt(1)
	v_mul_f32_e32 v109, v109, v99
	v_fmac_f32_e32 v109, v108, v98
	v_mul_f32_e32 v108, v111, v95
	v_fmac_f32_e32 v108, v110, v94
	v_add_f32_e32 v108, v109, v108
	s_waitcnt lgkmcnt(0)
	v_mul_f32_e32 v113, v113, v97
	v_add_f32_e32 v116, v116, v108
	v_fmac_f32_e32 v113, v112, v96
	v_mul_f32_e32 v112, v115, v93
	ds_read_b128 v[108:111], v1 offset:53248
	v_fmac_f32_e32 v112, v114, v92
	v_add_f32_e32 v112, v113, v112
	v_add_f32_e32 v116, v116, v112
	ds_read_b128 v[112:115], v1 offset:54272
	s_waitcnt lgkmcnt(1)
	v_mul_f32_e32 v109, v109, v91
	v_fmac_f32_e32 v109, v108, v90
	v_mul_f32_e32 v108, v111, v87
	v_fmac_f32_e32 v108, v110, v86
	v_add_f32_e32 v108, v109, v108
	s_waitcnt lgkmcnt(0)
	v_mul_f32_e32 v113, v113, v89
	v_add_f32_e32 v116, v116, v108
	v_fmac_f32_e32 v113, v112, v88
	v_mul_f32_e32 v112, v115, v85
	ds_read_b128 v[108:111], v1 offset:55296
	v_fmac_f32_e32 v112, v114, v84
	v_add_f32_e32 v112, v113, v112
	v_add_f32_e32 v116, v116, v112
	ds_read_b128 v[112:115], v1 offset:56320
	s_waitcnt lgkmcnt(1)
	v_mul_f32_e32 v109, v109, v83
	v_fmac_f32_e32 v109, v108, v82
	v_mul_f32_e32 v108, v111, v79
	v_fmac_f32_e32 v108, v110, v78
	v_add_f32_e32 v108, v109, v108
	s_waitcnt lgkmcnt(0)
	v_mul_f32_e32 v109, v113, v81
	v_mul_f32_e32 v110, v115, v77
	v_fmac_f32_e32 v109, v112, v80
	v_fmac_f32_e32 v110, v114, v76
	v_add_f32_e32 v108, v116, v108
	v_add_f32_e32 v109, v109, v110
	v_add_f32_e32 v108, v108, v109
	v_mov_b32_e32 v109, 0
	v_mov_b32_e32 v113, 0
	v_add_f32_dpp v108, v108, v108 quad_perm:[1,0,3,2] row_mask:0xf bank_mask:0xf bound_ctrl:1
	s_nop 1
	v_add_f32_dpp v108, v108, v108 quad_perm:[2,3,0,1] row_mask:0xf bank_mask:0xf bound_ctrl:1
	s_nop 1
	v_add_f32_dpp v108, v108, v108 row_half_mirror row_mask:0xf bank_mask:0xf bound_ctrl:1
	s_nop 1
	v_add_f32_dpp v108, v108, v108 row_mirror row_mask:0xf bank_mask:0xf bound_ctrl:1
	s_nop 1
	v_mov_b32_dpp v109, v108 row_bcast:15 row_mask:0xa bank_mask:0xf
	v_add_f32_e32 v112, v108, v109
	ds_read_b128 v[108:111], v1 offset:57344
	s_nop 0
	v_mov_b32_dpp v113, v112 row_bcast:31 row_mask:0xc bank_mask:0xf
	v_add_f32_e32 v112, v112, v113
	s_nop 0
	v_readlane_b32 s55, v112, 63
	ds_read_b128 v[112:115], v1 offset:58368
	s_waitcnt lgkmcnt(1)
	v_mul_f32_e32 v107, v109, v107
	v_mul_f32_e32 v103, v111, v103
	v_fmac_f32_e32 v107, v108, v106
	v_fmac_f32_e32 v103, v110, v102
	v_add_f32_e32 v102, v107, v103
	s_waitcnt lgkmcnt(0)
	v_mul_f32_e32 v107, v113, v105
	v_mul_f32_e32 v101, v115, v101
	v_add_f32_e32 v106, 0, v102
	v_fmac_f32_e32 v107, v112, v104
	ds_read_b128 v[102:105], v1 offset:59392
	v_fmac_f32_e32 v101, v114, v100
	v_add_f32_e32 v100, v107, v101
	v_add_f32_e32 v100, v106, v100
	ds_read_b128 v[106:109], v1 offset:60416
	s_waitcnt lgkmcnt(1)
	v_mul_f32_e32 v99, v103, v99
	v_mul_f32_e32 v95, v105, v95
	v_fmac_f32_e32 v99, v102, v98
	v_fmac_f32_e32 v95, v104, v94
	v_add_f32_e32 v94, v99, v95
	s_waitcnt lgkmcnt(0)
	v_mul_f32_e32 v99, v107, v97
	v_mul_f32_e32 v93, v109, v93
	v_add_f32_e32 v98, v100, v94
	v_fmac_f32_e32 v99, v106, v96
	ds_read_b128 v[94:97], v1 offset:61440
	v_fmac_f32_e32 v93, v108, v92
	v_add_f32_e32 v92, v99, v93
	v_add_f32_e32 v92, v98, v92
	ds_read_b128 v[98:101], v1 offset:62464
	s_waitcnt lgkmcnt(1)
	v_mul_f32_e32 v91, v95, v91
	v_mul_f32_e32 v87, v97, v87
	v_fmac_f32_e32 v91, v94, v90
	v_fmac_f32_e32 v87, v96, v86
	v_add_f32_e32 v86, v91, v87
	s_waitcnt lgkmcnt(0)
	v_mul_f32_e32 v91, v99, v89
	v_mul_f32_e32 v85, v101, v85
	v_add_f32_e32 v90, v92, v86
	v_fmac_f32_e32 v91, v98, v88
	ds_read_b128 v[86:89], v1 offset:63488
	v_fmac_f32_e32 v85, v100, v84
	v_add_f32_e32 v84, v91, v85
	v_add_f32_e32 v84, v90, v84
	ds_read_b128 v[90:93], v1 offset:64512
	s_waitcnt lgkmcnt(1)
	v_mul_f32_e32 v83, v87, v83
	v_mul_f32_e32 v79, v89, v79
	v_fmac_f32_e32 v83, v86, v82
	v_fmac_f32_e32 v79, v88, v78
	v_add_f32_e32 v78, v83, v79
	s_waitcnt lgkmcnt(0)
	v_mul_f32_e32 v79, v91, v81
	v_mul_f32_e32 v77, v93, v77
	v_fmac_f32_e32 v79, v90, v80
	v_fmac_f32_e32 v77, v92, v76
	v_add_f32_e32 v78, v84, v78
	v_add_f32_e32 v76, v79, v77
	v_add_f32_e32 v76, v78, v76
	v_mov_b32_e32 v77, 0
	s_nop 0
	v_add_f32_dpp v76, v76, v76 quad_perm:[1,0,3,2] row_mask:0xf bank_mask:0xf bound_ctrl:1
	s_nop 1
	v_add_f32_dpp v76, v76, v76 quad_perm:[2,3,0,1] row_mask:0xf bank_mask:0xf bound_ctrl:1
	s_nop 1
	v_add_f32_dpp v76, v76, v76 row_half_mirror row_mask:0xf bank_mask:0xf bound_ctrl:1
	s_nop 1
	v_add_f32_dpp v76, v76, v76 row_mirror row_mask:0xf bank_mask:0xf bound_ctrl:1
	s_nop 1
	v_mov_b32_dpp v77, v76 row_bcast:15 row_mask:0xa bank_mask:0xf
	v_add_f32_e32 v76, v76, v77
	v_mov_b32_e32 v77, 0
	s_nop 1
	v_mov_b32_dpp v77, v76 row_bcast:31 row_mask:0xc bank_mask:0xf
	v_add_f32_e32 v76, v76, v77
	s_nop 0
	v_readlane_b32 s56, v76, 63
	s_and_saveexec_b64 s[38:39], s[4:5]
	s_cbranch_execz .LBB0_2187
	v_mov_b32_e32 v76, s16
	v_mov_b32_e32 v77, s17
	v_cmp_gt_f32_e64 s[2:3], s17, v76
	s_mov_b64 s[14:15], exec
	s_nop 0
	v_cndmask_b32_e64 v76, v76, v77, s[2:3]
	v_mov_b32_e32 v77, s35
	v_cmp_gt_f32_e64 s[6:7], s35, v76
	s_nop 1
	v_cndmask_b32_e64 v76, v76, v77, s[6:7]
	v_mov_b32_e32 v77, s52
	v_cmp_gt_f32_e64 s[8:9], s52, v76
	s_nop 1
	v_cndmask_b32_e64 v76, v76, v77, s[8:9]
	v_mov_b32_e32 v77, s53
	v_cmp_gt_f32_e64 s[10:11], s53, v76
	s_nop 1
	v_cndmask_b32_e64 v76, v76, v77, s[10:11]
	v_mov_b32_e32 v77, s54
	v_cmp_gt_f32_e64 s[12:13], s54, v76
	s_nop 1
	v_cndmask_b32_e64 v76, v76, v77, s[12:13]
	v_mov_b32_e32 v77, s55
	v_cmp_gt_f32_e64 s[0:1], s55, v76
	s_nop 1
	v_cndmask_b32_e64 v77, v76, v77, s[0:1]
	v_cndmask_b32_e64 v76, 0, 1, s[2:3]
	s_and_b64 s[2:3], s[6:7], exec
	v_readfirstlane_b32 s2, v76
	s_cselect_b32 s6, 2, s2
	s_and_b64 s[2:3], s[8:9], exec
	s_cselect_b32 s6, 3, s6
	s_and_b64 s[2:3], s[10:11], exec
	s_cselect_b32 s6, 4, s6
	s_and_b64 s[2:3], s[12:13], exec
	v_cmp_ngt_f32_e32 vcc, s56, v77
	s_cselect_b32 s6, 5, s6
	s_and_b64 s[2:3], s[0:1], exec
	v_mbcnt_lo_u32_b32 v76, s14, 0
	s_cselect_b32 s6, 6, s6
	s_and_b64 s[2:3], vcc, exec
	v_mbcnt_hi_u32_b32 v76, s15, v76
	s_cselect_b32 s57, s6, 7
	v_cmp_eq_u32_e64 s[2:3], 0, v76
	s_and_saveexec_b64 s[6:7], s[2:3]
	s_cbranch_execz .LBB0_2193
	s_lshl_b32 s2, s57, 2
	s_add_i32 s2, s2, 0
	s_add_i32 s2, s2, 0x25f20
	s_bcnt1_i32_b64 s3, s[14:15]
	v_mov_b32_e32 v78, s2
	v_mov_b32_e32 v79, s3
	ds_add_rtn_u32 v78, v78, v79
